# baseline (speedup 1.0000x reference)
_ZN12_GLOBAL__N_113search_kernelEPKfS1_PhPf:
	s_load_dwordx2 s[8:9], s[0:1], 0x0
	s_load_dwordx2 s[4:5], s[0:1], 0x10
	s_movk_i32 s3, 0x90
	v_readfirstlane_b32 s10, v0
	v_cmp_gt_u32_e32 vcc, s3, v0
	s_and_saveexec_b64 s[6:7], vcc
	v_mov_b32_e32 v2, -1
	v_lshlrev_b32_e32 v1, 3, v0
	v_mov_b32_e32 v3, v2
	ds_write_b64 v1, v[2:3] offset:16384
	s_or_b64 exec, exec, s[6:7]
	s_waitcnt lgkmcnt(0)
	s_add_u32 s6, s4, 0x240000
	s_addc_u32 s7, s5, 0
	s_lshl_b32 s11, s2, 1
	s_and_b32 s14, s11, 14
	s_ashr_i32 s11, s2, 7
	s_lshr_b32 s15, s10, 6
	s_add_i32 s14, s14, s11
	s_bfe_u32 s2, s2, 0x40003
	s_mul_i32 s11, s15, 24
	v_mul_u32_u24_e32 v2, 0x71d, v0
	v_mul_u32_u24_e32 v4, 0x195, v0
	s_min_u32 s18, s11, 0xa5
	s_mul_i32 s11, s14, 3
	s_mul_i32 s12, s2, 9
	s_mov_b32 s13, 0
	v_lshrrev_b32_e32 v3, 16, v2
	s_movk_i32 s19, 0xffdc
	v_lshrrev_b32_e32 v5, 17, v4
	v_mad_i32_i24 v2, v3, s19, v0
	v_mad_i32_i24 v4, v5, -9, v3
	v_add_u32_e32 v3, s11, v5
	v_mov_b64_e32 v[6:7], s[12:13]
	v_mad_i64_i32 v[8:9], s[16:17], v3, s3, v[6:7]
	v_ashrrev_i32_e32 v5, 31, v4
	v_lshl_add_u64 v[4:5], v[8:9], 0, v[4:5]
	s_movk_i32 s13, 0x240
	v_mov_b64_e32 v[8:9], s[8:9]
	v_mad_u64_u32 v[10:11], s[8:9], v4, s13, v[8:9]
	v_min_u32_e32 v4, 0x1cb, v0
	v_or_b32_e32 v4, 0x200, v4
	v_mad_i32_i24 v11, v5, s13, v11
	v_mul_u32_u24_e32 v5, 0x71d, v4
	v_ashrrev_i32_e32 v3, 31, v2
	v_lshrrev_b32_e32 v5, 16, v5
	v_lshl_add_u64 v[2:3], v[2:3], 4, v[10:11]
	v_mad_i32_i24 v10, v5, s19, v4
	v_mul_u32_u24_e32 v4, 0x653, v4
	v_lshrrev_b32_e32 v11, 19, v4
	v_mad_i32_i24 v4, v11, -9, v5
	v_add_u32_e32 v5, s11, v11
	v_mad_i64_i32 v[6:7], s[8:9], v5, s3, v[6:7]
	v_ashrrev_i32_e32 v5, 31, v4
	v_lshl_add_u64 v[4:5], v[6:7], 0, v[4:5]
	v_mad_u64_u32 v[12:13], s[8:9], v4, s13, v[8:9]
	s_mul_i32 s8, s14, 0x90
	s_barrier
	s_load_dwordx2 s[42:43], s[0:1], 0x8
	s_load_dwordx2 s[62:63], s[0:1], 0x0
	v_mov_b32_e32 v244, v2
	v_mov_b32_e32 v245, v3
	global_load_dwordx4 v[6:9], v[2:3], off
	v_mad_i32_i24 v13, v5, s13, v13
	v_ashrrev_i32_e32 v11, 31, v10
	v_lshl_add_u64 v[10:11], v[10:11], 4, v[12:13]
	v_mov_b32_e32 v246, v10
	v_mov_b32_e32 v247, v11
	global_load_dwordx4 v[10:13], v[10:11], off
	v_and_b32_e32 v1, 63, v0
	s_add_i32 s20, s8, s12
	s_lshl_b32 s20, s20, 10
	v_lshl_add_u32 v164, v1, 4, s20
	s_mul_i32 s9, s14, 0xbd
	s_add_i32 s21, s9, s18
	s_lshl_b32 s21, s21, 10
	v_lshl_add_u32 v165, v1, 4, s21
	s_add_u32 s22, s4, 0x1000
	s_addc_u32 s23, s5, 0
	s_add_u32 s24, s4, 0x2000
	s_addc_u32 s25, s5, 0
	s_mov_b32 s26, s6
	s_mov_b32 s27, s7
	s_add_u32 s28, s6, 0x1000
	s_addc_u32 s29, s7, 0
	s_add_u32 s30, s6, 0x2000
	s_addc_u32 s31, s7, 0
	s_add_u32 s32, s6, 0x3000
	s_addc_u32 s33, s7, 0
	s_add_u32 s34, s6, 0x4000
	s_addc_u32 s35, s7, 0
	s_add_u32 s36, s6, 0x5000
	s_addc_u32 s37, s7, 0
	v_bfe_u32 v166, v0, 4, 2
	v_and_b32_e32 v167, 15, v0
	v_lshlrev_b32_e32 v167, 3, v167
	s_mul_i32 s40, s15, 6
	s_mov_b32 s41, 0x7f000000
	global_load_dwordx4 v[112:115], v164, s[4:5]
	global_load_dwordx4 v[16:19], v165, s[26:27] nt
	global_load_dwordx4 v[20:23], v165, s[26:27] offset:1024 nt
	global_load_dwordx4 v[24:27], v165, s[26:27] offset:2048 nt
	global_load_dwordx4 v[28:31], v165, s[26:27] offset:3072 nt
	global_load_dwordx4 v[32:35], v165, s[28:29] nt
	global_load_dwordx4 v[36:39], v165, s[28:29] offset:1024 nt
	global_load_dwordx4 v[40:43], v165, s[28:29] offset:2048 nt
	global_load_dwordx4 v[44:47], v165, s[28:29] offset:3072 nt
	global_load_dwordx4 v[48:51], v165, s[30:31] nt
	global_load_dwordx4 v[52:55], v165, s[30:31] offset:1024 nt
	global_load_dwordx4 v[56:59], v165, s[30:31] offset:2048 nt
	global_load_dwordx4 v[60:63], v165, s[30:31] offset:3072 nt
	global_load_dwordx4 v[64:67], v165, s[32:33] nt
	global_load_dwordx4 v[68:71], v165, s[32:33] offset:1024 nt
	global_load_dwordx4 v[72:75], v165, s[32:33] offset:2048 nt
	global_load_dwordx4 v[76:79], v165, s[32:33] offset:3072 nt
	global_load_dwordx4 v[80:83], v165, s[34:35] nt
	global_load_dwordx4 v[84:87], v165, s[34:35] offset:1024 nt
	global_load_dwordx4 v[88:91], v165, s[34:35] offset:2048 nt
	global_load_dwordx4 v[92:95], v165, s[34:35] offset:3072 nt
	global_load_dwordx4 v[96:99], v165, s[36:37] nt
	global_load_dwordx4 v[100:103], v165, s[36:37] offset:1024 nt
	global_load_dwordx4 v[104:107], v165, s[36:37] offset:2048 nt
	global_load_dwordx4 v[108:111], v165, s[36:37] offset:3072 nt
	global_load_dwordx4 v[116:119], v164, s[4:5] offset:1024
	v_lshlrev_b32_e32 v14, 4, v0
	s_lshr_b32 s50, s15, 1
	s_and_b32 s51, s15, 1
	s_lshl_b32 s51, s51, 3
	s_mov_b32 s48, 0x1010101
	s_mov_b32 s49, 0x1010101
	s_movk_i32 s58, 0x900
	s_movk_i32 s59, 0xb40
	v_and_b32_e32 v168, 7, v0
	v_lshrrev_b32_e32 v177, 3, v1
	v_or_b32_e32 v177, s51, v177
	v_lshlrev_b32_e32 v169, 3, v177
	v_and_b32_e32 v179, 3, v0
	v_lshlrev_b32_e32 v179, 8, v179
	v_lshl_add_u32 v170, v177, 4, v179
	v_add_u32_e32 v170, s20, v170
	v_lshrrev_b32_e32 v179, 2, v168
	v_and_b32_e32 v180, 3, v0
	v_lshl_or_b32 v171, v179, 4, v180
	v_mul_u32_u24_e32 v179, 11, v168
	v_lshrrev_b32_e32 v179, 5, v179
	v_mul_u32_u24_e32 v180, 3, v179
	v_sub_u32_e32 v180, v168, v180
	v_mul_u32_u24_e32 v181, 0x90, v179
	v_add_u32_e32 v181, v181, v180
	v_mul_u32_u24_e32 v172, 0x240, v181
	v_mul_u32_u24_e32 v181, 0x48, v179
	v_add_u32_e32 v181, v181, v180
	v_mul_u32_u24_e32 v173, 0x120, v181
	v_mul_u32_u24_e32 v181, 0x24, v179
	v_add_u32_e32 v181, v181, v180
	v_mul_u32_u24_e32 v174, 0x90, v181
	v_mul_u32_u24_e32 v181, 9, v179
	v_add_u32_e32 v181, v181, v180
	v_mul_u32_u24_e32 v175, 0x240, v181
	v_add_u32_e32 v176, 8, v168
	v_mov_b32_e32 v248, 0
	v_mov_b32_e32 v253, 0x900
	v_mov_b32_e32 v254, 0x240
	s_waitcnt lgkmcnt(0)
	s_mul_i32 s60, s14, 0x3cc00
	s_add_u32 s42, s42, s60
	s_addc_u32 s43, s43, 0
	s_mul_i32 s60, s14, 0xf300
	s_add_u32 s44, s4, s60
	s_addc_u32 s45, s5, 0
	s_add_u32 s44, s44, 0x534000
	s_addc_u32 s45, s45, 0
	s_mul_i32 s60, s14, 0x3cc0
	s_add_u32 s46, s4, s60
	s_addc_u32 s47, s5, 0
	s_add_u32 s46, s46, 0x627000
	s_addc_u32 s47, s47, 0
	v_mov_b32_e32 v152, s42
	v_mov_b32_e32 v153, s43
	v_mov_b32_e32 v154, s44
	v_mov_b32_e32 v155, s45
	v_mov_b32_e32 v159, s46
	v_mov_b32_e32 v161, s47
	s_sub_u32 s60, s42, s62
	s_subb_u32 s61, s43, s63
	s_mul_i32 s62, s14, 0x3cc00
	s_sub_u32 s60, s60, s62
	s_subb_u32 s61, s61, 0
	v_lshl_add_u64 v[244:245], v[244:245], 0, s[60:61]
	v_lshl_add_u64 v[246:247], v[246:247], 0, s[60:61]
	s_lshl_b32 s62, s15, 10
	s_add_i32 s62, s62, 0x46e0
	s_mov_b32 m0, s62
	s_mul_i32 s62, s2, 0xf30
	s_add_u32 s60, s44, s62
	s_addc_u32 s61, s45, 0
	v_lshlrev_b32_e32 v240, 4, v0
	v_mov_b32_e32 v241, 0
	v_lshl_add_u64 v[240:241], v[240:241], 0, s[60:61]
	s_mul_i32 s62, s2, 0x3cc
	s_add_u32 s60, s46, s62
	s_addc_u32 s61, s47, 0
	v_lshlrev_b32_e32 v242, 2, v0
	v_mov_b32_e32 v243, 0
	v_lshl_add_u64 v[242:243], v[242:243], 0, s[60:61]
	global_load_lds_dwordx4 v[244:245], off
	global_load_lds_dwordx4 v[246:247], off
	global_load_lds_dwordx4 v[240:241], off
	global_load_lds_dword v[242:243], off
	s_waitcnt vmcnt(25)
	ds_write_b128 v14, v[6:9]
	ds_write_b128 v14, v[10:13] offset:8192
	v_mfma_f32_16x16x32_f16 v[120:123], v[16:19], v[112:115], 0
	v_mfma_f32_16x16x32_f16 v[124:127], v[20:23], v[112:115], 0
	v_mfma_f32_16x16x32_f16 v[128:131], v[24:27], v[112:115], 0
	v_mfma_f32_16x16x32_f16 v[132:135], v[28:31], v[112:115], 0
	s_waitcnt vmcnt(21)
	v_mfma_f32_16x16x32_f16 v[136:139], v[32:35], v[112:115], 0
	v_mfma_f32_16x16x32_f16 v[140:143], v[36:39], v[112:115], 0
	v_mfma_f32_16x16x32_f16 v[144:147], v[40:43], v[112:115], 0
	v_mfma_f32_16x16x32_f16 v[148:151], v[44:47], v[112:115], 0
	v_min3_i32 v160, v120, v121, s41
	v_min3_i32 v160, v122, v123, v160
	v_min3_i32 v160, v124, v125, v160
	v_min3_i32 v160, v126, v127, v160
	v_min3_i32 v160, v128, v129, v160
	v_min3_i32 v160, v130, v131, v160
	v_min3_i32 v160, v132, v133, v160
	v_min3_i32 v157, v134, v135, v160
	s_waitcnt vmcnt(17)
	v_mfma_f32_16x16x32_f16 v[120:123], v[48:51], v[112:115], 0
	v_mfma_f32_16x16x32_f16 v[124:127], v[52:55], v[112:115], 0
	v_mov_b32_e32 v158, 0
	v_mfma_f32_16x16x32_f16 v[128:131], v[56:59], v[112:115], 0
	v_mfma_f32_16x16x32_f16 v[132:135], v[60:63], v[112:115], 0
	v_min3_i32 v160, v136, v137, v157
	v_min3_i32 v160, v138, v139, v160
	v_min3_i32 v160, v140, v141, v160
	v_min3_i32 v160, v142, v143, v160
	v_min3_i32 v160, v144, v145, v160
	v_min3_i32 v160, v146, v147, v160
	v_min3_i32 v160, v148, v149, v160
	v_min3_i32 v156, v150, v151, v160
	v_cmp_ge_i32_e32 vcc, v156, v157
	s_waitcnt vmcnt(13)
	v_mfma_f32_16x16x32_f16 v[136:139], v[64:67], v[112:115], 0
	v_mfma_f32_16x16x32_f16 v[140:143], v[68:71], v[112:115], 0
	v_cndmask_b32_e32 v158, 1, v158, vcc
	v_mfma_f32_16x16x32_f16 v[144:147], v[72:75], v[112:115], 0
	v_mfma_f32_16x16x32_f16 v[148:151], v[76:79], v[112:115], 0
	v_min3_i32 v160, v120, v121, v156
	v_min3_i32 v160, v122, v123, v160
	v_min3_i32 v160, v124, v125, v160
	v_min3_i32 v160, v126, v127, v160
	v_min3_i32 v160, v128, v129, v160
	v_min3_i32 v160, v130, v131, v160
	v_min3_i32 v160, v132, v133, v160
	v_min3_i32 v157, v134, v135, v160
	v_cmp_ge_i32_e32 vcc, v157, v156
	s_waitcnt vmcnt(9)
	v_mfma_f32_16x16x32_f16 v[120:123], v[80:83], v[112:115], 0
	v_mfma_f32_16x16x32_f16 v[124:127], v[84:87], v[112:115], 0
	v_cndmask_b32_e32 v158, 2, v158, vcc
	v_mfma_f32_16x16x32_f16 v[128:131], v[88:91], v[112:115], 0
	v_mfma_f32_16x16x32_f16 v[132:135], v[92:95], v[112:115], 0
	v_min3_i32 v160, v136, v137, v157
	v_min3_i32 v160, v138, v139, v160
	v_min3_i32 v160, v140, v141, v160
	v_min3_i32 v160, v142, v143, v160
	v_min3_i32 v160, v144, v145, v160
	v_min3_i32 v160, v146, v147, v160
	v_min3_i32 v160, v148, v149, v160
	v_min3_i32 v156, v150, v151, v160
	v_cmp_ge_i32_e32 vcc, v156, v157
	s_waitcnt vmcnt(5)
	v_mfma_f32_16x16x32_f16 v[136:139], v[96:99], v[112:115], 0
	v_mfma_f32_16x16x32_f16 v[140:143], v[100:103], v[112:115], 0
	v_cndmask_b32_e32 v158, 3, v158, vcc
	v_mfma_f32_16x16x32_f16 v[144:147], v[104:107], v[112:115], 0
	v_mfma_f32_16x16x32_f16 v[148:151], v[108:111], v[112:115], 0
	v_min3_i32 v160, v120, v121, v156
	v_min3_i32 v160, v122, v123, v160
	v_min3_i32 v160, v124, v125, v160
	v_min3_i32 v160, v126, v127, v160
	v_min3_i32 v160, v128, v129, v160
	v_min3_i32 v160, v130, v131, v160
	v_min3_i32 v160, v132, v133, v160
	v_min3_i32 v157, v134, v135, v160
	v_cmp_ge_i32_e32 vcc, v157, v156
	s_waitcnt vmcnt(4)
	global_load_dwordx4 v[112:115], v164, s[4:5] offset:2048
	v_mfma_f32_16x16x32_f16 v[120:123], v[16:19], v[116:119], 0
	v_mfma_f32_16x16x32_f16 v[124:127], v[20:23], v[116:119], 0
	v_cndmask_b32_e32 v158, 4, v158, vcc
	v_mfma_f32_16x16x32_f16 v[128:131], v[24:27], v[116:119], 0
	v_mfma_f32_16x16x32_f16 v[132:135], v[28:31], v[116:119], 0
	v_min3_i32 v160, v136, v137, v157
	v_min3_i32 v160, v138, v139, v160
	v_min3_i32 v160, v140, v141, v160
	v_min3_i32 v160, v142, v143, v160
	v_min3_i32 v160, v144, v145, v160
	v_min3_i32 v160, v146, v147, v160
	v_min3_i32 v160, v148, v149, v160
	v_min3_i32 v156, v150, v151, v160
	v_cmp_ge_i32_e32 vcc, v156, v157
	v_mfma_f32_16x16x32_f16 v[136:139], v[32:35], v[116:119], 0
	v_mfma_f32_16x16x32_f16 v[140:143], v[36:39], v[116:119], 0
	v_cndmask_b32_e32 v158, 5, v158, vcc
	v_add_u32_e32 v162, s40, v158
	v_lshl_or_b32 v162, v162, 2, v166
	v_mov_b32_e32 v163, v156
	ds_min_u64 v167, v[162:163] offset:16384
	v_mfma_f32_16x16x32_f16 v[144:147], v[40:43], v[116:119], 0
	v_mfma_f32_16x16x32_f16 v[148:151], v[44:47], v[116:119], 0
	v_min3_i32 v160, v120, v121, s41
	v_min3_i32 v160, v122, v123, v160
	v_min3_i32 v160, v124, v125, v160
	v_min3_i32 v160, v126, v127, v160
	v_min3_i32 v160, v128, v129, v160
	v_min3_i32 v160, v130, v131, v160
	v_min3_i32 v160, v132, v133, v160
	v_min3_i32 v157, v134, v135, v160
	v_mfma_f32_16x16x32_f16 v[120:123], v[48:51], v[116:119], 0
	v_mfma_f32_16x16x32_f16 v[124:127], v[52:55], v[116:119], 0
	v_mov_b32_e32 v158, 0
	v_mfma_f32_16x16x32_f16 v[128:131], v[56:59], v[116:119], 0
	v_mfma_f32_16x16x32_f16 v[132:135], v[60:63], v[116:119], 0
	v_min3_i32 v160, v136, v137, v157
	v_min3_i32 v160, v138, v139, v160
	v_min3_i32 v160, v140, v141, v160
	v_min3_i32 v160, v142, v143, v160
	v_min3_i32 v160, v144, v145, v160
	v_min3_i32 v160, v146, v147, v160
	v_min3_i32 v160, v148, v149, v160
	v_min3_i32 v156, v150, v151, v160
	v_cmp_ge_i32_e32 vcc, v156, v157
	v_mfma_f32_16x16x32_f16 v[136:139], v[64:67], v[116:119], 0
	v_mfma_f32_16x16x32_f16 v[140:143], v[68:71], v[116:119], 0
	v_cndmask_b32_e32 v158, 1, v158, vcc
	v_mfma_f32_16x16x32_f16 v[144:147], v[72:75], v[116:119], 0
	v_mfma_f32_16x16x32_f16 v[148:151], v[76:79], v[116:119], 0
	v_min3_i32 v160, v120, v121, v156
	v_min3_i32 v160, v122, v123, v160
	v_min3_i32 v160, v124, v125, v160
	v_min3_i32 v160, v126, v127, v160
	v_min3_i32 v160, v128, v129, v160
	v_min3_i32 v160, v130, v131, v160
	v_min3_i32 v160, v132, v133, v160
	v_min3_i32 v157, v134, v135, v160
	v_cmp_ge_i32_e32 vcc, v157, v156
	v_mfma_f32_16x16x32_f16 v[120:123], v[80:83], v[116:119], 0
	v_mfma_f32_16x16x32_f16 v[124:127], v[84:87], v[116:119], 0
	v_cndmask_b32_e32 v158, 2, v158, vcc
	v_mfma_f32_16x16x32_f16 v[128:131], v[88:91], v[116:119], 0
	v_mfma_f32_16x16x32_f16 v[132:135], v[92:95], v[116:119], 0
	v_min3_i32 v160, v136, v137, v157
	v_min3_i32 v160, v138, v139, v160
	v_min3_i32 v160, v140, v141, v160
	v_min3_i32 v160, v142, v143, v160
	v_min3_i32 v160, v144, v145, v160
	v_min3_i32 v160, v146, v147, v160
	v_min3_i32 v160, v148, v149, v160
	v_min3_i32 v156, v150, v151, v160
	v_cmp_ge_i32_e32 vcc, v156, v157
	v_mfma_f32_16x16x32_f16 v[136:139], v[96:99], v[116:119], 0
	v_mfma_f32_16x16x32_f16 v[140:143], v[100:103], v[116:119], 0
	v_cndmask_b32_e32 v158, 3, v158, vcc
	v_mfma_f32_16x16x32_f16 v[144:147], v[104:107], v[116:119], 0
	v_mfma_f32_16x16x32_f16 v[148:151], v[108:111], v[116:119], 0
	v_min3_i32 v160, v120, v121, v156
	v_min3_i32 v160, v122, v123, v160
	v_min3_i32 v160, v124, v125, v160
	v_min3_i32 v160, v126, v127, v160
	v_min3_i32 v160, v128, v129, v160
	v_min3_i32 v160, v130, v131, v160
	v_min3_i32 v160, v132, v133, v160
	v_min3_i32 v157, v134, v135, v160
	v_cmp_ge_i32_e32 vcc, v157, v156
	s_waitcnt vmcnt(0)
	global_load_dwordx4 v[116:119], v164, s[4:5] offset:3072
	v_mfma_f32_16x16x32_f16 v[120:123], v[16:19], v[112:115], 0
	v_mfma_f32_16x16x32_f16 v[124:127], v[20:23], v[112:115], 0
	v_cndmask_b32_e32 v158, 4, v158, vcc
	v_mfma_f32_16x16x32_f16 v[128:131], v[24:27], v[112:115], 0
	v_mfma_f32_16x16x32_f16 v[132:135], v[28:31], v[112:115], 0
	v_min3_i32 v160, v136, v137, v157
	v_min3_i32 v160, v138, v139, v160
	v_min3_i32 v160, v140, v141, v160
	v_min3_i32 v160, v142, v143, v160
	v_min3_i32 v160, v144, v145, v160
	v_min3_i32 v160, v146, v147, v160
	v_min3_i32 v160, v148, v149, v160
	v_min3_i32 v156, v150, v151, v160
	v_cmp_ge_i32_e32 vcc, v156, v157
	v_mfma_f32_16x16x32_f16 v[136:139], v[32:35], v[112:115], 0
	v_mfma_f32_16x16x32_f16 v[140:143], v[36:39], v[112:115], 0
	v_cndmask_b32_e32 v158, 5, v158, vcc
	v_add_u32_e32 v162, s40, v158
	v_lshl_or_b32 v162, v162, 2, v166
	v_mov_b32_e32 v163, v156
	ds_min_u64 v167, v[162:163] offset:16512
	v_mfma_f32_16x16x32_f16 v[144:147], v[40:43], v[112:115], 0
	v_mfma_f32_16x16x32_f16 v[148:151], v[44:47], v[112:115], 0
	v_min3_i32 v160, v120, v121, s41
	v_min3_i32 v160, v122, v123, v160
	v_min3_i32 v160, v124, v125, v160
	v_min3_i32 v160, v126, v127, v160
	v_min3_i32 v160, v128, v129, v160
	v_min3_i32 v160, v130, v131, v160
	v_min3_i32 v160, v132, v133, v160
	v_min3_i32 v157, v134, v135, v160
	v_mfma_f32_16x16x32_f16 v[120:123], v[48:51], v[112:115], 0
	v_mfma_f32_16x16x32_f16 v[124:127], v[52:55], v[112:115], 0
	v_mov_b32_e32 v158, 0
	v_mfma_f32_16x16x32_f16 v[128:131], v[56:59], v[112:115], 0
	v_mfma_f32_16x16x32_f16 v[132:135], v[60:63], v[112:115], 0
	v_min3_i32 v160, v136, v137, v157
	v_min3_i32 v160, v138, v139, v160
	v_min3_i32 v160, v140, v141, v160
	v_min3_i32 v160, v142, v143, v160
	v_min3_i32 v160, v144, v145, v160
	v_min3_i32 v160, v146, v147, v160
	v_min3_i32 v160, v148, v149, v160
	v_min3_i32 v156, v150, v151, v160
	v_cmp_ge_i32_e32 vcc, v156, v157
	v_mfma_f32_16x16x32_f16 v[136:139], v[64:67], v[112:115], 0
	v_mfma_f32_16x16x32_f16 v[140:143], v[68:71], v[112:115], 0
	v_cndmask_b32_e32 v158, 1, v158, vcc
	v_mfma_f32_16x16x32_f16 v[144:147], v[72:75], v[112:115], 0
	v_mfma_f32_16x16x32_f16 v[148:151], v[76:79], v[112:115], 0
	v_min3_i32 v160, v120, v121, v156
	v_min3_i32 v160, v122, v123, v160
	v_min3_i32 v160, v124, v125, v160
	v_min3_i32 v160, v126, v127, v160
	v_min3_i32 v160, v128, v129, v160
	v_min3_i32 v160, v130, v131, v160
	v_min3_i32 v160, v132, v133, v160
	v_min3_i32 v157, v134, v135, v160
	v_cmp_ge_i32_e32 vcc, v157, v156
	v_mfma_f32_16x16x32_f16 v[120:123], v[80:83], v[112:115], 0
	v_mfma_f32_16x16x32_f16 v[124:127], v[84:87], v[112:115], 0
	v_cndmask_b32_e32 v158, 2, v158, vcc
	v_mfma_f32_16x16x32_f16 v[128:131], v[88:91], v[112:115], 0
	v_mfma_f32_16x16x32_f16 v[132:135], v[92:95], v[112:115], 0
	v_min3_i32 v160, v136, v137, v157
	v_min3_i32 v160, v138, v139, v160
	v_min3_i32 v160, v140, v141, v160
	v_min3_i32 v160, v142, v143, v160
	v_min3_i32 v160, v144, v145, v160
	v_min3_i32 v160, v146, v147, v160
	v_min3_i32 v160, v148, v149, v160
	v_min3_i32 v156, v150, v151, v160
	v_cmp_ge_i32_e32 vcc, v156, v157
	v_mfma_f32_16x16x32_f16 v[136:139], v[96:99], v[112:115], 0
	v_mfma_f32_16x16x32_f16 v[140:143], v[100:103], v[112:115], 0
	v_cndmask_b32_e32 v158, 3, v158, vcc
	v_mfma_f32_16x16x32_f16 v[144:147], v[104:107], v[112:115], 0
	v_mfma_f32_16x16x32_f16 v[148:151], v[108:111], v[112:115], 0
	v_min3_i32 v160, v120, v121, v156
	v_min3_i32 v160, v122, v123, v160
	v_min3_i32 v160, v124, v125, v160
	v_min3_i32 v160, v126, v127, v160
	v_min3_i32 v160, v128, v129, v160
	v_min3_i32 v160, v130, v131, v160
	v_min3_i32 v160, v132, v133, v160
	v_min3_i32 v157, v134, v135, v160
	v_cmp_ge_i32_e32 vcc, v157, v156
	s_waitcnt vmcnt(0)
	global_load_dwordx4 v[112:115], v164, s[22:23]
	v_mfma_f32_16x16x32_f16 v[120:123], v[16:19], v[116:119], 0
	v_mfma_f32_16x16x32_f16 v[124:127], v[20:23], v[116:119], 0
	v_cndmask_b32_e32 v158, 4, v158, vcc
	v_mfma_f32_16x16x32_f16 v[128:131], v[24:27], v[116:119], 0
	v_mfma_f32_16x16x32_f16 v[132:135], v[28:31], v[116:119], 0
	v_min3_i32 v160, v136, v137, v157
	v_min3_i32 v160, v138, v139, v160
	v_min3_i32 v160, v140, v141, v160
	v_min3_i32 v160, v142, v143, v160
	v_min3_i32 v160, v144, v145, v160
	v_min3_i32 v160, v146, v147, v160
	v_min3_i32 v160, v148, v149, v160
	v_min3_i32 v156, v150, v151, v160
	v_cmp_ge_i32_e32 vcc, v156, v157
	v_mfma_f32_16x16x32_f16 v[136:139], v[32:35], v[116:119], 0
	v_mfma_f32_16x16x32_f16 v[140:143], v[36:39], v[116:119], 0
	v_cndmask_b32_e32 v158, 5, v158, vcc
	v_add_u32_e32 v162, s40, v158
	v_lshl_or_b32 v162, v162, 2, v166
	v_mov_b32_e32 v163, v156
	ds_min_u64 v167, v[162:163] offset:16640
	v_mfma_f32_16x16x32_f16 v[144:147], v[40:43], v[116:119], 0
	v_mfma_f32_16x16x32_f16 v[148:151], v[44:47], v[116:119], 0
	v_min3_i32 v160, v120, v121, s41
	v_min3_i32 v160, v122, v123, v160
	v_min3_i32 v160, v124, v125, v160
	v_min3_i32 v160, v126, v127, v160
	v_min3_i32 v160, v128, v129, v160
	v_min3_i32 v160, v130, v131, v160
	v_min3_i32 v160, v132, v133, v160
	v_min3_i32 v157, v134, v135, v160
	v_mfma_f32_16x16x32_f16 v[120:123], v[48:51], v[116:119], 0
	v_mfma_f32_16x16x32_f16 v[124:127], v[52:55], v[116:119], 0
	v_mov_b32_e32 v158, 0
	v_mfma_f32_16x16x32_f16 v[128:131], v[56:59], v[116:119], 0
	v_mfma_f32_16x16x32_f16 v[132:135], v[60:63], v[116:119], 0
	v_min3_i32 v160, v136, v137, v157
	v_min3_i32 v160, v138, v139, v160
	v_min3_i32 v160, v140, v141, v160
	v_min3_i32 v160, v142, v143, v160
	v_min3_i32 v160, v144, v145, v160
	v_min3_i32 v160, v146, v147, v160
	v_min3_i32 v160, v148, v149, v160
	v_min3_i32 v156, v150, v151, v160
	v_cmp_ge_i32_e32 vcc, v156, v157
	v_mfma_f32_16x16x32_f16 v[136:139], v[64:67], v[116:119], 0
	v_mfma_f32_16x16x32_f16 v[140:143], v[68:71], v[116:119], 0
	v_cndmask_b32_e32 v158, 1, v158, vcc
	v_mfma_f32_16x16x32_f16 v[144:147], v[72:75], v[116:119], 0
	v_mfma_f32_16x16x32_f16 v[148:151], v[76:79], v[116:119], 0
	v_min3_i32 v160, v120, v121, v156
	v_min3_i32 v160, v122, v123, v160
	v_min3_i32 v160, v124, v125, v160
	v_min3_i32 v160, v126, v127, v160
	v_min3_i32 v160, v128, v129, v160
	v_min3_i32 v160, v130, v131, v160
	v_min3_i32 v160, v132, v133, v160
	v_min3_i32 v157, v134, v135, v160
	v_cmp_ge_i32_e32 vcc, v157, v156
	v_mfma_f32_16x16x32_f16 v[120:123], v[80:83], v[116:119], 0
	v_mfma_f32_16x16x32_f16 v[124:127], v[84:87], v[116:119], 0
	v_cndmask_b32_e32 v158, 2, v158, vcc
	v_mfma_f32_16x16x32_f16 v[128:131], v[88:91], v[116:119], 0
	v_mfma_f32_16x16x32_f16 v[132:135], v[92:95], v[116:119], 0
	v_min3_i32 v160, v136, v137, v157
	v_min3_i32 v160, v138, v139, v160
	v_min3_i32 v160, v140, v141, v160
	v_min3_i32 v160, v142, v143, v160
	v_min3_i32 v160, v144, v145, v160
	v_min3_i32 v160, v146, v147, v160
	v_min3_i32 v160, v148, v149, v160
	v_min3_i32 v156, v150, v151, v160
	v_cmp_ge_i32_e32 vcc, v156, v157
	v_mfma_f32_16x16x32_f16 v[136:139], v[96:99], v[116:119], 0
	v_mfma_f32_16x16x32_f16 v[140:143], v[100:103], v[116:119], 0
	v_cndmask_b32_e32 v158, 3, v158, vcc
	v_mfma_f32_16x16x32_f16 v[144:147], v[104:107], v[116:119], 0
	v_mfma_f32_16x16x32_f16 v[148:151], v[108:111], v[116:119], 0
	v_min3_i32 v160, v120, v121, v156
	v_min3_i32 v160, v122, v123, v160
	v_min3_i32 v160, v124, v125, v160
	v_min3_i32 v160, v126, v127, v160
	v_min3_i32 v160, v128, v129, v160
	v_min3_i32 v160, v130, v131, v160
	v_min3_i32 v160, v132, v133, v160
	v_min3_i32 v157, v134, v135, v160
	v_cmp_ge_i32_e32 vcc, v157, v156
	s_waitcnt vmcnt(0)
	global_load_dwordx4 v[116:119], v164, s[22:23] offset:1024
	v_mfma_f32_16x16x32_f16 v[120:123], v[16:19], v[112:115], 0
	v_mfma_f32_16x16x32_f16 v[124:127], v[20:23], v[112:115], 0
	v_cndmask_b32_e32 v158, 4, v158, vcc
	v_mfma_f32_16x16x32_f16 v[128:131], v[24:27], v[112:115], 0
	v_mfma_f32_16x16x32_f16 v[132:135], v[28:31], v[112:115], 0
	v_min3_i32 v160, v136, v137, v157
	v_min3_i32 v160, v138, v139, v160
	v_min3_i32 v160, v140, v141, v160
	v_min3_i32 v160, v142, v143, v160
	v_min3_i32 v160, v144, v145, v160
	v_min3_i32 v160, v146, v147, v160
	v_min3_i32 v160, v148, v149, v160
	v_min3_i32 v156, v150, v151, v160
	v_cmp_ge_i32_e32 vcc, v156, v157
	v_mfma_f32_16x16x32_f16 v[136:139], v[32:35], v[112:115], 0
	v_mfma_f32_16x16x32_f16 v[140:143], v[36:39], v[112:115], 0
	v_cndmask_b32_e32 v158, 5, v158, vcc
	v_add_u32_e32 v162, s40, v158
	v_lshl_or_b32 v162, v162, 2, v166
	v_mov_b32_e32 v163, v156
	ds_min_u64 v167, v[162:163] offset:16768
	v_mfma_f32_16x16x32_f16 v[144:147], v[40:43], v[112:115], 0
	v_mfma_f32_16x16x32_f16 v[148:151], v[44:47], v[112:115], 0
	v_min3_i32 v160, v120, v121, s41
	v_min3_i32 v160, v122, v123, v160
	v_min3_i32 v160, v124, v125, v160
	v_min3_i32 v160, v126, v127, v160
	v_min3_i32 v160, v128, v129, v160
	v_min3_i32 v160, v130, v131, v160
	v_min3_i32 v160, v132, v133, v160
	v_min3_i32 v157, v134, v135, v160
	v_mfma_f32_16x16x32_f16 v[120:123], v[48:51], v[112:115], 0
	v_mfma_f32_16x16x32_f16 v[124:127], v[52:55], v[112:115], 0
	v_mov_b32_e32 v158, 0
	v_mfma_f32_16x16x32_f16 v[128:131], v[56:59], v[112:115], 0
	v_mfma_f32_16x16x32_f16 v[132:135], v[60:63], v[112:115], 0
	v_min3_i32 v160, v136, v137, v157
	v_min3_i32 v160, v138, v139, v160
	v_min3_i32 v160, v140, v141, v160
	v_min3_i32 v160, v142, v143, v160
	v_min3_i32 v160, v144, v145, v160
	v_min3_i32 v160, v146, v147, v160
	v_min3_i32 v160, v148, v149, v160
	v_min3_i32 v156, v150, v151, v160
	v_cmp_ge_i32_e32 vcc, v156, v157
	v_mfma_f32_16x16x32_f16 v[136:139], v[64:67], v[112:115], 0
	v_mfma_f32_16x16x32_f16 v[140:143], v[68:71], v[112:115], 0
	v_cndmask_b32_e32 v158, 1, v158, vcc
	v_mfma_f32_16x16x32_f16 v[144:147], v[72:75], v[112:115], 0
	v_mfma_f32_16x16x32_f16 v[148:151], v[76:79], v[112:115], 0
	v_min3_i32 v160, v120, v121, v156
	v_min3_i32 v160, v122, v123, v160
	v_min3_i32 v160, v124, v125, v160
	v_min3_i32 v160, v126, v127, v160
	v_min3_i32 v160, v128, v129, v160
	v_min3_i32 v160, v130, v131, v160
	v_min3_i32 v160, v132, v133, v160
	v_min3_i32 v157, v134, v135, v160
	v_cmp_ge_i32_e32 vcc, v157, v156
	v_mfma_f32_16x16x32_f16 v[120:123], v[80:83], v[112:115], 0
	v_mfma_f32_16x16x32_f16 v[124:127], v[84:87], v[112:115], 0
	v_cndmask_b32_e32 v158, 2, v158, vcc
	v_mfma_f32_16x16x32_f16 v[128:131], v[88:91], v[112:115], 0
	v_mfma_f32_16x16x32_f16 v[132:135], v[92:95], v[112:115], 0
	v_min3_i32 v160, v136, v137, v157
	v_min3_i32 v160, v138, v139, v160
	v_min3_i32 v160, v140, v141, v160
	v_min3_i32 v160, v142, v143, v160
	v_min3_i32 v160, v144, v145, v160
	v_min3_i32 v160, v146, v147, v160
	v_min3_i32 v160, v148, v149, v160
	v_min3_i32 v156, v150, v151, v160
	v_cmp_ge_i32_e32 vcc, v156, v157
	v_mfma_f32_16x16x32_f16 v[136:139], v[96:99], v[112:115], 0
	v_mfma_f32_16x16x32_f16 v[140:143], v[100:103], v[112:115], 0
	v_cndmask_b32_e32 v158, 3, v158, vcc
	v_mfma_f32_16x16x32_f16 v[144:147], v[104:107], v[112:115], 0
	v_mfma_f32_16x16x32_f16 v[148:151], v[108:111], v[112:115], 0
	v_min3_i32 v160, v120, v121, v156
	v_min3_i32 v160, v122, v123, v160
	v_min3_i32 v160, v124, v125, v160
	v_min3_i32 v160, v126, v127, v160
	v_min3_i32 v160, v128, v129, v160
	v_min3_i32 v160, v130, v131, v160
	v_min3_i32 v160, v132, v133, v160
	v_min3_i32 v157, v134, v135, v160
	v_cmp_ge_i32_e32 vcc, v157, v156
	s_waitcnt vmcnt(0)
	global_load_dwordx4 v[112:115], v164, s[22:23] offset:2048
	v_mfma_f32_16x16x32_f16 v[120:123], v[16:19], v[116:119], 0
	v_mfma_f32_16x16x32_f16 v[124:127], v[20:23], v[116:119], 0
	v_cndmask_b32_e32 v158, 4, v158, vcc
	v_mfma_f32_16x16x32_f16 v[128:131], v[24:27], v[116:119], 0
	v_mfma_f32_16x16x32_f16 v[132:135], v[28:31], v[116:119], 0
	v_min3_i32 v160, v136, v137, v157
	v_min3_i32 v160, v138, v139, v160
	v_min3_i32 v160, v140, v141, v160
	v_min3_i32 v160, v142, v143, v160
	v_min3_i32 v160, v144, v145, v160
	v_min3_i32 v160, v146, v147, v160
	v_min3_i32 v160, v148, v149, v160
	v_min3_i32 v156, v150, v151, v160
	v_cmp_ge_i32_e32 vcc, v156, v157
	v_mfma_f32_16x16x32_f16 v[136:139], v[32:35], v[116:119], 0
	v_mfma_f32_16x16x32_f16 v[140:143], v[36:39], v[116:119], 0
	v_cndmask_b32_e32 v158, 5, v158, vcc
	v_add_u32_e32 v162, s40, v158
	v_lshl_or_b32 v162, v162, 2, v166
	v_mov_b32_e32 v163, v156
	ds_min_u64 v167, v[162:163] offset:16896
	v_mfma_f32_16x16x32_f16 v[144:147], v[40:43], v[116:119], 0
	v_mfma_f32_16x16x32_f16 v[148:151], v[44:47], v[116:119], 0
	v_min3_i32 v160, v120, v121, s41
	v_min3_i32 v160, v122, v123, v160
	v_min3_i32 v160, v124, v125, v160
	v_min3_i32 v160, v126, v127, v160
	v_min3_i32 v160, v128, v129, v160
	v_min3_i32 v160, v130, v131, v160
	v_min3_i32 v160, v132, v133, v160
	v_min3_i32 v157, v134, v135, v160
	v_mfma_f32_16x16x32_f16 v[120:123], v[48:51], v[116:119], 0
	v_mfma_f32_16x16x32_f16 v[124:127], v[52:55], v[116:119], 0
	v_mov_b32_e32 v158, 0
	v_mfma_f32_16x16x32_f16 v[128:131], v[56:59], v[116:119], 0
	v_mfma_f32_16x16x32_f16 v[132:135], v[60:63], v[116:119], 0
	v_min3_i32 v160, v136, v137, v157
	v_min3_i32 v160, v138, v139, v160
	v_min3_i32 v160, v140, v141, v160
	v_min3_i32 v160, v142, v143, v160
	v_min3_i32 v160, v144, v145, v160
	v_min3_i32 v160, v146, v147, v160
	v_min3_i32 v160, v148, v149, v160
	v_min3_i32 v156, v150, v151, v160
	v_cmp_ge_i32_e32 vcc, v156, v157
	v_mfma_f32_16x16x32_f16 v[136:139], v[64:67], v[116:119], 0
	v_mfma_f32_16x16x32_f16 v[140:143], v[68:71], v[116:119], 0
	v_cndmask_b32_e32 v158, 1, v158, vcc
	v_mfma_f32_16x16x32_f16 v[144:147], v[72:75], v[116:119], 0
	v_mfma_f32_16x16x32_f16 v[148:151], v[76:79], v[116:119], 0
	v_min3_i32 v160, v120, v121, v156
	v_min3_i32 v160, v122, v123, v160
	v_min3_i32 v160, v124, v125, v160
	v_min3_i32 v160, v126, v127, v160
	v_min3_i32 v160, v128, v129, v160
	v_min3_i32 v160, v130, v131, v160
	v_min3_i32 v160, v132, v133, v160
	v_min3_i32 v157, v134, v135, v160
	v_cmp_ge_i32_e32 vcc, v157, v156
	v_mfma_f32_16x16x32_f16 v[120:123], v[80:83], v[116:119], 0
	v_mfma_f32_16x16x32_f16 v[124:127], v[84:87], v[116:119], 0
	v_cndmask_b32_e32 v158, 2, v158, vcc
	v_mfma_f32_16x16x32_f16 v[128:131], v[88:91], v[116:119], 0
	v_mfma_f32_16x16x32_f16 v[132:135], v[92:95], v[116:119], 0
	v_min3_i32 v160, v136, v137, v157
	v_min3_i32 v160, v138, v139, v160
	v_min3_i32 v160, v140, v141, v160
	v_min3_i32 v160, v142, v143, v160
	v_min3_i32 v160, v144, v145, v160
	v_min3_i32 v160, v146, v147, v160
	v_min3_i32 v160, v148, v149, v160
	v_min3_i32 v156, v150, v151, v160
	v_cmp_ge_i32_e32 vcc, v156, v157
	v_mfma_f32_16x16x32_f16 v[136:139], v[96:99], v[116:119], 0
	v_mfma_f32_16x16x32_f16 v[140:143], v[100:103], v[116:119], 0
	v_cndmask_b32_e32 v158, 3, v158, vcc
	v_mfma_f32_16x16x32_f16 v[144:147], v[104:107], v[116:119], 0
	v_mfma_f32_16x16x32_f16 v[148:151], v[108:111], v[116:119], 0
	v_min3_i32 v160, v120, v121, v156
	v_min3_i32 v160, v122, v123, v160
	v_min3_i32 v160, v124, v125, v160
	v_min3_i32 v160, v126, v127, v160
	v_min3_i32 v160, v128, v129, v160
	v_min3_i32 v160, v130, v131, v160
	v_min3_i32 v160, v132, v133, v160
	v_min3_i32 v157, v134, v135, v160
	v_cmp_ge_i32_e32 vcc, v157, v156
	s_waitcnt vmcnt(0)
	global_load_dwordx4 v[116:119], v164, s[22:23] offset:3072
	v_mfma_f32_16x16x32_f16 v[120:123], v[16:19], v[112:115], 0
	v_mfma_f32_16x16x32_f16 v[124:127], v[20:23], v[112:115], 0
	v_cndmask_b32_e32 v158, 4, v158, vcc
	v_mfma_f32_16x16x32_f16 v[128:131], v[24:27], v[112:115], 0
	v_mfma_f32_16x16x32_f16 v[132:135], v[28:31], v[112:115], 0
	v_min3_i32 v160, v136, v137, v157
	v_min3_i32 v160, v138, v139, v160
	v_min3_i32 v160, v140, v141, v160
	v_min3_i32 v160, v142, v143, v160
	v_min3_i32 v160, v144, v145, v160
	v_min3_i32 v160, v146, v147, v160
	v_min3_i32 v160, v148, v149, v160
	v_min3_i32 v156, v150, v151, v160
	v_cmp_ge_i32_e32 vcc, v156, v157
	v_mfma_f32_16x16x32_f16 v[136:139], v[32:35], v[112:115], 0
	v_mfma_f32_16x16x32_f16 v[140:143], v[36:39], v[112:115], 0
	v_cndmask_b32_e32 v158, 5, v158, vcc
	v_add_u32_e32 v162, s40, v158
	v_lshl_or_b32 v162, v162, 2, v166
	v_mov_b32_e32 v163, v156
	ds_min_u64 v167, v[162:163] offset:17024
	v_mfma_f32_16x16x32_f16 v[144:147], v[40:43], v[112:115], 0
	v_mfma_f32_16x16x32_f16 v[148:151], v[44:47], v[112:115], 0
	v_min3_i32 v160, v120, v121, s41
	v_min3_i32 v160, v122, v123, v160
	v_min3_i32 v160, v124, v125, v160
	v_min3_i32 v160, v126, v127, v160
	v_min3_i32 v160, v128, v129, v160
	v_min3_i32 v160, v130, v131, v160
	v_min3_i32 v160, v132, v133, v160
	v_min3_i32 v157, v134, v135, v160
	v_mfma_f32_16x16x32_f16 v[120:123], v[48:51], v[112:115], 0
	v_mfma_f32_16x16x32_f16 v[124:127], v[52:55], v[112:115], 0
	v_mov_b32_e32 v158, 0
	v_mfma_f32_16x16x32_f16 v[128:131], v[56:59], v[112:115], 0
	v_mfma_f32_16x16x32_f16 v[132:135], v[60:63], v[112:115], 0
	v_min3_i32 v160, v136, v137, v157
	v_min3_i32 v160, v138, v139, v160
	v_min3_i32 v160, v140, v141, v160
	v_min3_i32 v160, v142, v143, v160
	v_min3_i32 v160, v144, v145, v160
	v_min3_i32 v160, v146, v147, v160
	v_min3_i32 v160, v148, v149, v160
	v_min3_i32 v156, v150, v151, v160
	v_cmp_ge_i32_e32 vcc, v156, v157
	v_mfma_f32_16x16x32_f16 v[136:139], v[64:67], v[112:115], 0
	v_mfma_f32_16x16x32_f16 v[140:143], v[68:71], v[112:115], 0
	v_cndmask_b32_e32 v158, 1, v158, vcc
	v_mfma_f32_16x16x32_f16 v[144:147], v[72:75], v[112:115], 0
	v_mfma_f32_16x16x32_f16 v[148:151], v[76:79], v[112:115], 0
	v_min3_i32 v160, v120, v121, v156
	v_min3_i32 v160, v122, v123, v160
	v_min3_i32 v160, v124, v125, v160
	v_min3_i32 v160, v126, v127, v160
	v_min3_i32 v160, v128, v129, v160
	v_min3_i32 v160, v130, v131, v160
	v_min3_i32 v160, v132, v133, v160
	v_min3_i32 v157, v134, v135, v160
	v_cmp_ge_i32_e32 vcc, v157, v156
	v_mfma_f32_16x16x32_f16 v[120:123], v[80:83], v[112:115], 0
	v_mfma_f32_16x16x32_f16 v[124:127], v[84:87], v[112:115], 0
	v_cndmask_b32_e32 v158, 2, v158, vcc
	v_mfma_f32_16x16x32_f16 v[128:131], v[88:91], v[112:115], 0
	v_mfma_f32_16x16x32_f16 v[132:135], v[92:95], v[112:115], 0
	v_min3_i32 v160, v136, v137, v157
	v_min3_i32 v160, v138, v139, v160
	v_min3_i32 v160, v140, v141, v160
	v_min3_i32 v160, v142, v143, v160
	v_min3_i32 v160, v144, v145, v160
	v_min3_i32 v160, v146, v147, v160
	v_min3_i32 v160, v148, v149, v160
	v_min3_i32 v156, v150, v151, v160
	v_cmp_ge_i32_e32 vcc, v156, v157
	v_mfma_f32_16x16x32_f16 v[136:139], v[96:99], v[112:115], 0
	v_mfma_f32_16x16x32_f16 v[140:143], v[100:103], v[112:115], 0
	v_cndmask_b32_e32 v158, 3, v158, vcc
	v_mfma_f32_16x16x32_f16 v[144:147], v[104:107], v[112:115], 0
	v_mfma_f32_16x16x32_f16 v[148:151], v[108:111], v[112:115], 0
	v_min3_i32 v160, v120, v121, v156
	v_min3_i32 v160, v122, v123, v160
	v_min3_i32 v160, v124, v125, v160
	v_min3_i32 v160, v126, v127, v160
	v_min3_i32 v160, v128, v129, v160
	v_min3_i32 v160, v130, v131, v160
	v_min3_i32 v160, v132, v133, v160
	v_min3_i32 v157, v134, v135, v160
	v_cmp_ge_i32_e32 vcc, v157, v156
	s_waitcnt vmcnt(0)
	global_load_dwordx4 v[112:115], v164, s[24:25]
	v_mfma_f32_16x16x32_f16 v[120:123], v[16:19], v[116:119], 0
	v_mfma_f32_16x16x32_f16 v[124:127], v[20:23], v[116:119], 0
	v_cndmask_b32_e32 v158, 4, v158, vcc
	v_mfma_f32_16x16x32_f16 v[128:131], v[24:27], v[116:119], 0
	v_mfma_f32_16x16x32_f16 v[132:135], v[28:31], v[116:119], 0
	v_min3_i32 v160, v136, v137, v157
	v_min3_i32 v160, v138, v139, v160
	v_min3_i32 v160, v140, v141, v160
	v_min3_i32 v160, v142, v143, v160
	v_min3_i32 v160, v144, v145, v160
	v_min3_i32 v160, v146, v147, v160
	v_min3_i32 v160, v148, v149, v160
	v_min3_i32 v156, v150, v151, v160
	v_cmp_ge_i32_e32 vcc, v156, v157
	v_mfma_f32_16x16x32_f16 v[136:139], v[32:35], v[116:119], 0
	v_mfma_f32_16x16x32_f16 v[140:143], v[36:39], v[116:119], 0
	v_cndmask_b32_e32 v158, 5, v158, vcc
	v_add_u32_e32 v162, s40, v158
	v_lshl_or_b32 v162, v162, 2, v166
	v_mov_b32_e32 v163, v156
	ds_min_u64 v167, v[162:163] offset:17152
	v_mfma_f32_16x16x32_f16 v[144:147], v[40:43], v[116:119], 0
	v_mfma_f32_16x16x32_f16 v[148:151], v[44:47], v[116:119], 0
	v_min3_i32 v160, v120, v121, s41
	v_min3_i32 v160, v122, v123, v160
	v_min3_i32 v160, v124, v125, v160
	v_min3_i32 v160, v126, v127, v160
	v_min3_i32 v160, v128, v129, v160
	v_min3_i32 v160, v130, v131, v160
	v_min3_i32 v160, v132, v133, v160
	v_min3_i32 v157, v134, v135, v160
	v_mfma_f32_16x16x32_f16 v[120:123], v[48:51], v[116:119], 0
	v_mfma_f32_16x16x32_f16 v[124:127], v[52:55], v[116:119], 0
	v_mov_b32_e32 v158, 0
	v_mfma_f32_16x16x32_f16 v[128:131], v[56:59], v[116:119], 0
	v_mfma_f32_16x16x32_f16 v[132:135], v[60:63], v[116:119], 0
	v_min3_i32 v160, v136, v137, v157
	v_min3_i32 v160, v138, v139, v160
	v_min3_i32 v160, v140, v141, v160
	v_min3_i32 v160, v142, v143, v160
	v_min3_i32 v160, v144, v145, v160
	v_min3_i32 v160, v146, v147, v160
	v_min3_i32 v160, v148, v149, v160
	v_min3_i32 v156, v150, v151, v160
	v_cmp_ge_i32_e32 vcc, v156, v157
	v_mfma_f32_16x16x32_f16 v[136:139], v[64:67], v[116:119], 0
	v_mfma_f32_16x16x32_f16 v[140:143], v[68:71], v[116:119], 0
	v_cndmask_b32_e32 v158, 1, v158, vcc
	v_mfma_f32_16x16x32_f16 v[144:147], v[72:75], v[116:119], 0
	v_mfma_f32_16x16x32_f16 v[148:151], v[76:79], v[116:119], 0
	v_min3_i32 v160, v120, v121, v156
	v_min3_i32 v160, v122, v123, v160
	v_min3_i32 v160, v124, v125, v160
	v_min3_i32 v160, v126, v127, v160
	v_min3_i32 v160, v128, v129, v160
	v_min3_i32 v160, v130, v131, v160
	v_min3_i32 v160, v132, v133, v160
	v_min3_i32 v157, v134, v135, v160
	v_cmp_ge_i32_e32 vcc, v157, v156
	v_mfma_f32_16x16x32_f16 v[120:123], v[80:83], v[116:119], 0
	v_mfma_f32_16x16x32_f16 v[124:127], v[84:87], v[116:119], 0
	v_cndmask_b32_e32 v158, 2, v158, vcc
	v_mfma_f32_16x16x32_f16 v[128:131], v[88:91], v[116:119], 0
	v_mfma_f32_16x16x32_f16 v[132:135], v[92:95], v[116:119], 0
	v_min3_i32 v160, v136, v137, v157
	v_min3_i32 v160, v138, v139, v160
	v_min3_i32 v160, v140, v141, v160
	v_min3_i32 v160, v142, v143, v160
	v_min3_i32 v160, v144, v145, v160
	v_min3_i32 v160, v146, v147, v160
	v_min3_i32 v160, v148, v149, v160
	v_min3_i32 v156, v150, v151, v160
	v_cmp_ge_i32_e32 vcc, v156, v157
	v_mfma_f32_16x16x32_f16 v[136:139], v[96:99], v[116:119], 0
	v_mfma_f32_16x16x32_f16 v[140:143], v[100:103], v[116:119], 0
	v_cndmask_b32_e32 v158, 3, v158, vcc
	v_mfma_f32_16x16x32_f16 v[144:147], v[104:107], v[116:119], 0
	v_mfma_f32_16x16x32_f16 v[148:151], v[108:111], v[116:119], 0
	v_min3_i32 v160, v120, v121, v156
	v_min3_i32 v160, v122, v123, v160
	v_min3_i32 v160, v124, v125, v160
	v_min3_i32 v160, v126, v127, v160
	v_min3_i32 v160, v128, v129, v160
	v_min3_i32 v160, v130, v131, v160
	v_min3_i32 v160, v132, v133, v160
	v_min3_i32 v157, v134, v135, v160
	v_cmp_ge_i32_e32 vcc, v157, v156
	s_waitcnt vmcnt(0)
	v_mfma_f32_16x16x32_f16 v[120:123], v[16:19], v[112:115], 0
	v_mfma_f32_16x16x32_f16 v[124:127], v[20:23], v[112:115], 0
	v_cndmask_b32_e32 v158, 4, v158, vcc
	v_mfma_f32_16x16x32_f16 v[128:131], v[24:27], v[112:115], 0
	v_mfma_f32_16x16x32_f16 v[132:135], v[28:31], v[112:115], 0
	v_min3_i32 v160, v136, v137, v157
	v_min3_i32 v160, v138, v139, v160
	v_min3_i32 v160, v140, v141, v160
	v_min3_i32 v160, v142, v143, v160
	v_min3_i32 v160, v144, v145, v160
	v_min3_i32 v160, v146, v147, v160
	v_min3_i32 v160, v148, v149, v160
	v_min3_i32 v156, v150, v151, v160
	v_cmp_ge_i32_e32 vcc, v156, v157
	v_mfma_f32_16x16x32_f16 v[136:139], v[32:35], v[112:115], 0
	v_mfma_f32_16x16x32_f16 v[140:143], v[36:39], v[112:115], 0
	v_cndmask_b32_e32 v158, 5, v158, vcc
	v_add_u32_e32 v162, s40, v158
	v_lshl_or_b32 v162, v162, 2, v166
	v_mov_b32_e32 v163, v156
	ds_min_u64 v167, v[162:163] offset:17280
	v_mfma_f32_16x16x32_f16 v[144:147], v[40:43], v[112:115], 0
	v_mfma_f32_16x16x32_f16 v[148:151], v[44:47], v[112:115], 0
	v_min3_i32 v160, v120, v121, s41
	v_min3_i32 v160, v122, v123, v160
	v_min3_i32 v160, v124, v125, v160
	v_min3_i32 v160, v126, v127, v160
	v_min3_i32 v160, v128, v129, v160
	v_min3_i32 v160, v130, v131, v160
	v_min3_i32 v160, v132, v133, v160
	v_min3_i32 v157, v134, v135, v160
	v_mfma_f32_16x16x32_f16 v[120:123], v[48:51], v[112:115], 0
	v_mfma_f32_16x16x32_f16 v[124:127], v[52:55], v[112:115], 0
	v_mov_b32_e32 v158, 0
	v_mfma_f32_16x16x32_f16 v[128:131], v[56:59], v[112:115], 0
	v_mfma_f32_16x16x32_f16 v[132:135], v[60:63], v[112:115], 0
	v_min3_i32 v160, v136, v137, v157
	v_min3_i32 v160, v138, v139, v160
	v_min3_i32 v160, v140, v141, v160
	v_min3_i32 v160, v142, v143, v160
	v_min3_i32 v160, v144, v145, v160
	v_min3_i32 v160, v146, v147, v160
	v_min3_i32 v160, v148, v149, v160
	v_min3_i32 v156, v150, v151, v160
	v_cmp_ge_i32_e32 vcc, v156, v157
	v_mfma_f32_16x16x32_f16 v[136:139], v[64:67], v[112:115], 0
	v_mfma_f32_16x16x32_f16 v[140:143], v[68:71], v[112:115], 0
	v_cndmask_b32_e32 v158, 1, v158, vcc
	v_mfma_f32_16x16x32_f16 v[144:147], v[72:75], v[112:115], 0
	v_mfma_f32_16x16x32_f16 v[148:151], v[76:79], v[112:115], 0
	v_min3_i32 v160, v120, v121, v156
	v_min3_i32 v160, v122, v123, v160
	v_min3_i32 v160, v124, v125, v160
	v_min3_i32 v160, v126, v127, v160
	v_min3_i32 v160, v128, v129, v160
	v_min3_i32 v160, v130, v131, v160
	v_min3_i32 v160, v132, v133, v160
	v_min3_i32 v157, v134, v135, v160
	v_cmp_ge_i32_e32 vcc, v157, v156
	v_mfma_f32_16x16x32_f16 v[120:123], v[80:83], v[112:115], 0
	v_mfma_f32_16x16x32_f16 v[124:127], v[84:87], v[112:115], 0
	v_cndmask_b32_e32 v158, 2, v158, vcc
	v_mfma_f32_16x16x32_f16 v[128:131], v[88:91], v[112:115], 0
	v_mfma_f32_16x16x32_f16 v[132:135], v[92:95], v[112:115], 0
	v_min3_i32 v160, v136, v137, v157
	v_min3_i32 v160, v138, v139, v160
	v_min3_i32 v160, v140, v141, v160
	v_min3_i32 v160, v142, v143, v160
	v_min3_i32 v160, v144, v145, v160
	v_min3_i32 v160, v146, v147, v160
	v_min3_i32 v160, v148, v149, v160
	v_min3_i32 v156, v150, v151, v160
	v_cmp_ge_i32_e32 vcc, v156, v157
	v_mfma_f32_16x16x32_f16 v[136:139], v[96:99], v[112:115], 0
	v_mfma_f32_16x16x32_f16 v[140:143], v[100:103], v[112:115], 0
	v_cndmask_b32_e32 v158, 3, v158, vcc
	v_mfma_f32_16x16x32_f16 v[144:147], v[104:107], v[112:115], 0
	v_mfma_f32_16x16x32_f16 v[148:151], v[108:111], v[112:115], 0
	v_min3_i32 v160, v120, v121, v156
	v_min3_i32 v160, v122, v123, v160
	v_min3_i32 v160, v124, v125, v160
	v_min3_i32 v160, v126, v127, v160
	v_min3_i32 v160, v128, v129, v160
	v_min3_i32 v160, v130, v131, v160
	v_min3_i32 v160, v132, v133, v160
	v_min3_i32 v157, v134, v135, v160
	v_cmp_ge_i32_e32 vcc, v157, v156
	s_nop 1
	v_cndmask_b32_e32 v158, 4, v158, vcc
	s_nop 7
	v_min3_i32 v160, v136, v137, v157
	v_min3_i32 v160, v138, v139, v160
	v_min3_i32 v160, v140, v141, v160
	v_min3_i32 v160, v142, v143, v160
	v_min3_i32 v160, v144, v145, v160
	v_min3_i32 v160, v146, v147, v160
	v_min3_i32 v160, v148, v149, v160
	v_min3_i32 v156, v150, v151, v160
	v_cmp_ge_i32_e32 vcc, v156, v157
	s_nop 1
	v_cndmask_b32_e32 v158, 5, v158, vcc
	v_add_u32_e32 v162, s40, v158
	v_lshl_or_b32 v162, v162, 2, v166
	v_mov_b32_e32 v163, v156
	ds_min_u64 v167, v[162:163] offset:17408
	s_waitcnt lgkmcnt(0)
	s_barrier
	s_mov_b32 s64, s50
	s_add_i32 s65, s50, 4
	s_mov_b32 s66, 8
	s_cmp_eq_u32 s50, 0
	s_cbranch_scc0 .Lno2a
	s_lshl_b32 s60, s66, 7
	v_add_u32_e32 v244, s60, v169
	ds_read_b32 v217, v244 offset:16384
	s_lshl_b32 s60, s66, 4
	v_add_u32_e32 v244, s60, v177
	v_mul_u32_u24_e32 v245, 0x556, v244
	v_lshrrev_b32_e32 v245, 16, v245
	v_mul_u32_u24_e32 v246, 48, v245
	v_sub_u32_e32 v246, v244, v246
	v_mul_u32_u24_e32 v245, 0x6c0, v245
	v_mad_u32_u24 v215, v246, 12, v245
	v_add_u32_e32 v215, v215, v175
	s_lshl_b32 s60, s66, 10
	v_add_u32_e32 v241, s60, v170
.Lno2a:
	s_lshl_b32 s60, s64, 7
	v_add_u32_e32 v244, s60, v169
	ds_read_b32 v55, v244 offset:16384
	s_lshl_b32 s60, s64, 4
	v_add_u32_e32 v244, s60, v177
	v_mul_u32_u24_e32 v245, 0x556, v244
	v_lshrrev_b32_e32 v245, 16, v245
	v_mul_u32_u24_e32 v246, 48, v245
	v_sub_u32_e32 v246, v244, v246
	v_mul_u32_u24_e32 v245, 0x6c0, v245
	v_mad_u32_u24 v53, v246, 12, v245
	v_add_u32_e32 v53, v53, v175
	s_lshl_b32 s60, s64, 10
	v_add_u32_e32 v79, s60, v170
	s_lshl_b32 s60, s65, 7
	v_add_u32_e32 v244, s60, v169
	ds_read_b32 v119, v244 offset:16384
	s_lshl_b32 s60, s65, 4
	v_add_u32_e32 v244, s60, v177
	v_mul_u32_u24_e32 v245, 0x556, v244
	v_lshrrev_b32_e32 v245, 16, v245
	v_mul_u32_u24_e32 v246, 48, v245
	v_sub_u32_e32 v246, v244, v246
	v_mul_u32_u24_e32 v245, 0x6c0, v245
	v_mad_u32_u24 v117, v246, 12, v245
	v_add_u32_e32 v117, v117, v175
	s_lshl_b32 s60, s65, 10
	v_add_u32_e32 v143, s60, v170
	s_waitcnt lgkmcnt(0)
	s_cmp_eq_u32 s50, 0
	s_cbranch_scc0 .Lno2b
	v_lshrrev_b32_e32 v244, 2, v217
	v_mul_u32_u24_e32 v245, 43, v244
	v_lshrrev_b32_e32 v245, 8, v245
	v_mul_u32_u24_e32 v246, 6, v245
	v_sub_u32_e32 v246, v244, v246
	v_mul_u32_u24_e32 v245, 24, v245
	v_min_u32_e32 v245, 0xa5, v245
	v_lshl_add_u32 v245, v246, 2, v245
	v_lshrrev_b32_e32 v246, 2, v168
	v_add_u32_e32 v245, v245, v246
	v_and_b32_e32 v246, 3, v217
	v_lshlrev_b32_e32 v246, 2, v246
	v_and_b32_e32 v247, 3, v168
	v_or_b32_e32 v246, v246, v247
	v_lshl_or_b32 v214, v245, 4, v246
	v_add_u32_e32 v245, s9, v245
	v_lshlrev_b32_e32 v246, 4, v246
	v_lshl_or_b32 v216, v245, 10, v246
	global_load_dwordx4 v[178:181], v216, s[6:7]
	global_load_dwordx4 v[194:197], v216, s[6:7] offset:2048
	global_load_dwordx4 v[182:185], v216, s[6:7] offset:256
	global_load_dwordx4 v[198:201], v216, s[6:7] offset:2304
	global_load_dwordx4 v[186:189], v216, s[6:7] offset:512
	global_load_dwordx4 v[202:205], v216, s[6:7] offset:2560
	global_load_dwordx4 v[190:193], v216, s[6:7] offset:768
	global_load_dwordx4 v[206:209], v216, s[6:7] offset:2816
	global_load_dwordx4 v[210:213], v241, s[4:5]
.Lno2b:
	v_lshrrev_b32_e32 v244, 2, v55
	v_mul_u32_u24_e32 v245, 43, v244
	v_lshrrev_b32_e32 v245, 8, v245
	v_mul_u32_u24_e32 v246, 6, v245
	v_sub_u32_e32 v246, v244, v246
	v_mul_u32_u24_e32 v245, 24, v245
	v_min_u32_e32 v245, 0xa5, v245
	v_lshl_add_u32 v245, v246, 2, v245
	v_lshrrev_b32_e32 v246, 2, v168
	v_add_u32_e32 v245, v245, v246
	v_and_b32_e32 v246, 3, v55
	v_lshlrev_b32_e32 v246, 2, v246
	v_and_b32_e32 v247, 3, v168
	v_or_b32_e32 v246, v246, v247
	v_lshl_or_b32 v52, v245, 4, v246
	v_add_u32_e32 v245, s9, v245
	v_lshlrev_b32_e32 v246, 4, v246
	v_lshl_or_b32 v54, v245, 10, v246
	global_load_dwordx4 v[16:19], v54, s[6:7]
	global_load_dwordx4 v[32:35], v54, s[6:7] offset:2048
	global_load_dwordx4 v[20:23], v54, s[6:7] offset:256
	global_load_dwordx4 v[36:39], v54, s[6:7] offset:2304
	global_load_dwordx4 v[24:27], v54, s[6:7] offset:512
	global_load_dwordx4 v[40:43], v54, s[6:7] offset:2560
	global_load_dwordx4 v[28:31], v54, s[6:7] offset:768
	global_load_dwordx4 v[44:47], v54, s[6:7] offset:2816
	global_load_dwordx4 v[48:51], v79, s[4:5]
	v_lshrrev_b32_e32 v244, 2, v119
	v_mul_u32_u24_e32 v245, 43, v244
	v_lshrrev_b32_e32 v245, 8, v245
	v_mul_u32_u24_e32 v246, 6, v245
	v_sub_u32_e32 v246, v244, v246
	v_mul_u32_u24_e32 v245, 24, v245
	v_min_u32_e32 v245, 0xa5, v245
	v_lshl_add_u32 v245, v246, 2, v245
	v_lshrrev_b32_e32 v246, 2, v168
	v_add_u32_e32 v245, v245, v246
	v_and_b32_e32 v246, 3, v119
	v_lshlrev_b32_e32 v246, 2, v246
	v_and_b32_e32 v247, 3, v168
	v_or_b32_e32 v246, v246, v247
	v_lshl_or_b32 v116, v245, 4, v246
	v_add_u32_e32 v245, s9, v245
	v_lshlrev_b32_e32 v246, 4, v246
	v_lshl_or_b32 v118, v245, 10, v246
	global_load_dwordx4 v[80:83], v118, s[6:7]
	global_load_dwordx4 v[96:99], v118, s[6:7] offset:2048
	global_load_dwordx4 v[84:87], v118, s[6:7] offset:256
	global_load_dwordx4 v[100:103], v118, s[6:7] offset:2304
	global_load_dwordx4 v[88:91], v118, s[6:7] offset:512
	global_load_dwordx4 v[104:107], v118, s[6:7] offset:2560
	global_load_dwordx4 v[92:95], v118, s[6:7] offset:768
	global_load_dwordx4 v[108:111], v118, s[6:7] offset:2816
	global_load_dwordx4 v[112:115], v143, s[4:5]
	s_cmp_eq_u32 s50, 0
	s_cbranch_scc0 .Lno2c
	s_waitcnt vmcnt(18)
	v_mov_b32_e32 v218, 0
	v_mov_b32_e32 v219, 0
	v_dot2c_f32_f16_dpp v218, v210, v178 quad_perm:[0,0,0,0] row_mask:0xf bank_mask:0xf
	v_dot2c_f32_f16_dpp v219, v210, v194 quad_perm:[0,0,0,0] row_mask:0xf bank_mask:0xf
	v_dot2c_f32_f16_dpp v218, v211, v179 quad_perm:[0,0,0,0] row_mask:0xf bank_mask:0xf
	v_dot2c_f32_f16_dpp v219, v211, v195 quad_perm:[0,0,0,0] row_mask:0xf bank_mask:0xf
	v_dot2c_f32_f16_dpp v218, v212, v180 quad_perm:[0,0,0,0] row_mask:0xf bank_mask:0xf
	v_dot2c_f32_f16_dpp v219, v212, v196 quad_perm:[0,0,0,0] row_mask:0xf bank_mask:0xf
	v_dot2c_f32_f16_dpp v218, v213, v181 quad_perm:[0,0,0,0] row_mask:0xf bank_mask:0xf
	v_dot2c_f32_f16_dpp v219, v213, v197 quad_perm:[0,0,0,0] row_mask:0xf bank_mask:0xf
	v_dot2c_f32_f16_dpp v218, v210, v182 quad_perm:[1,1,1,1] row_mask:0xf bank_mask:0xf
	v_dot2c_f32_f16_dpp v219, v210, v198 quad_perm:[1,1,1,1] row_mask:0xf bank_mask:0xf
	v_dot2c_f32_f16_dpp v218, v211, v183 quad_perm:[1,1,1,1] row_mask:0xf bank_mask:0xf
	v_dot2c_f32_f16_dpp v219, v211, v199 quad_perm:[1,1,1,1] row_mask:0xf bank_mask:0xf
	v_dot2c_f32_f16_dpp v218, v212, v184 quad_perm:[1,1,1,1] row_mask:0xf bank_mask:0xf
	v_dot2c_f32_f16_dpp v219, v212, v200 quad_perm:[1,1,1,1] row_mask:0xf bank_mask:0xf
	v_dot2c_f32_f16_dpp v218, v213, v185 quad_perm:[1,1,1,1] row_mask:0xf bank_mask:0xf
	v_dot2c_f32_f16_dpp v219, v213, v201 quad_perm:[1,1,1,1] row_mask:0xf bank_mask:0xf
	v_dot2c_f32_f16_dpp v218, v210, v186 quad_perm:[2,2,2,2] row_mask:0xf bank_mask:0xf
	v_dot2c_f32_f16_dpp v219, v210, v202 quad_perm:[2,2,2,2] row_mask:0xf bank_mask:0xf
	v_dot2c_f32_f16_dpp v218, v211, v187 quad_perm:[2,2,2,2] row_mask:0xf bank_mask:0xf
	v_dot2c_f32_f16_dpp v219, v211, v203 quad_perm:[2,2,2,2] row_mask:0xf bank_mask:0xf
	v_dot2c_f32_f16_dpp v218, v212, v188 quad_perm:[2,2,2,2] row_mask:0xf bank_mask:0xf
	v_dot2c_f32_f16_dpp v219, v212, v204 quad_perm:[2,2,2,2] row_mask:0xf bank_mask:0xf
	v_dot2c_f32_f16_dpp v218, v213, v189 quad_perm:[2,2,2,2] row_mask:0xf bank_mask:0xf
	v_dot2c_f32_f16_dpp v219, v213, v205 quad_perm:[2,2,2,2] row_mask:0xf bank_mask:0xf
	v_dot2c_f32_f16_dpp v218, v210, v190 quad_perm:[3,3,3,3] row_mask:0xf bank_mask:0xf
	v_dot2c_f32_f16_dpp v219, v210, v206 quad_perm:[3,3,3,3] row_mask:0xf bank_mask:0xf
	v_dot2c_f32_f16_dpp v218, v211, v191 quad_perm:[3,3,3,3] row_mask:0xf bank_mask:0xf
	v_dot2c_f32_f16_dpp v219, v211, v207 quad_perm:[3,3,3,3] row_mask:0xf bank_mask:0xf
	v_dot2c_f32_f16_dpp v218, v212, v192 quad_perm:[3,3,3,3] row_mask:0xf bank_mask:0xf
	v_dot2c_f32_f16_dpp v219, v212, v208 quad_perm:[3,3,3,3] row_mask:0xf bank_mask:0xf
	v_dot2c_f32_f16_dpp v218, v213, v193 quad_perm:[3,3,3,3] row_mask:0xf bank_mask:0xf
	v_dot2c_f32_f16_dpp v219, v213, v209 quad_perm:[3,3,3,3] row_mask:0xf bank_mask:0xf
	s_nop 2
	v_and_or_b32 v244, v218, -16, v168
	v_and_or_b32 v245, v219, -16, v176
	v_min_i32_e32 v220, v244, v245
	s_nop 1
	v_min_i32_dpp v220, v220, v220 quad_perm:[1,0,3,2] row_mask:0xf bank_mask:0xf bound_ctrl:1
	s_nop 1
	v_min_i32_dpp v220, v220, v220 quad_perm:[2,3,0,1] row_mask:0xf bank_mask:0xf bound_ctrl:1
	s_nop 1
	v_min_i32_dpp v220, v220, v220 row_half_mirror row_mask:0xf bank_mask:0xf bound_ctrl:1
	v_and_b32_e32 v244, 12, v220
	v_lshlrev_b32_e32 v244, 2, v244
	v_and_b32_e32 v245, 3, v220
	v_sub_u32_e32 v246, v214, v171
	v_add3_u32 v221, v246, v244, v245
	v_cmp_le_u32_e64 s[54:55], s58, v221
	v_cmp_le_u32_e64 s[56:57], s59, v221
	s_nop 1
	v_cndmask_b32_e64 v244, 0, v253, s[54:55]
	v_cndmask_b32_e64 v245, 0, v254, s[56:57]
	v_sub_u32_e32 v246, v221, v244
	v_sub_u32_e32 v246, v246, v245
	v_cndmask_b32_e64 v244, 0, 1, s[54:55]
	v_cndmask_b32_e64 v245, 0, 1, s[56:57]
	v_add_u32_e32 v247, v244, v245
	v_lshlrev_b32_e32 v244, v247, v246
	v_mul_u32_u24_e32 v244, 0xaab, v244
	v_lshrrev_b32_e32 v244, 17, v244
	v_mul_u32_u24_e32 v245, 0x60, v244
	v_lshrrev_b32_e32 v245, v247, v245
	v_add_u32_e32 v245, v246, v245
	v_mul_u32_u24_e32 v245, 12, v245
	v_cndmask_b32_e64 v244, v172, v173, s[54:55]
	v_cndmask_b32_e64 v244, v244, v174, s[56:57]
	v_add_u32_e32 v245, v245, v244
	v_cndmask_b32_e64 v244, v152, v154, s[54:55]
	v_cndmask_b32_e64 v244, v244, v159, s[56:57]
	v_cndmask_b32_e64 v246, v153, v155, s[54:55]
	v_cndmask_b32_e64 v246, v246, v161, s[56:57]
	v_add_co_u32_e64 v222, s[60:61], v244, v245
	s_nop 1
	v_addc_co_u32_e64 v223, s[60:61], 0, v246, s[60:61]
	v_sub_u32_e32 v244, 2, v247
	v_lshlrev_b32_e64 v244, v244, 36
	v_add_u32_e32 v246, 1, v244
	v_mul_u32_u24_e32 v244, v244, v246
	v_lshlrev_b32_e32 v244, 3, v244
	v_add_co_u32_e64 v224, s[60:61], v222, v244
	s_nop 1
	v_addc_co_u32_e64 v225, s[60:61], 0, v223, s[60:61]
	global_load_dwordx3 v[226:228], v[222:223], off
	ds_read_b32 v234, v215
	ds_read_b32 v235, v215 offset:4
	ds_read_b32 v236, v215 offset:8
	s_mov_b64 s[52:53], exec
	s_and_b64 exec, exec, s[48:49]
	global_load_dwordx3 v[230:232], v[224:225], off
	ds_read_b32 v238, v215 offset:11520
	ds_read_b32 v239, v215 offset:11524
	ds_read_b32 v240, v215 offset:11528
	s_mov_b64 exec, s[52:53]
.Lno2c:
	s_waitcnt vmcnt(9)
	v_mov_b32_e32 v56, 0
	v_mov_b32_e32 v57, 0
	v_dot2c_f32_f16_dpp v56, v48, v16 quad_perm:[0,0,0,0] row_mask:0xf bank_mask:0xf
	v_dot2c_f32_f16_dpp v57, v48, v32 quad_perm:[0,0,0,0] row_mask:0xf bank_mask:0xf
	v_dot2c_f32_f16_dpp v56, v49, v17 quad_perm:[0,0,0,0] row_mask:0xf bank_mask:0xf
	v_dot2c_f32_f16_dpp v57, v49, v33 quad_perm:[0,0,0,0] row_mask:0xf bank_mask:0xf
	v_dot2c_f32_f16_dpp v56, v50, v18 quad_perm:[0,0,0,0] row_mask:0xf bank_mask:0xf
	v_dot2c_f32_f16_dpp v57, v50, v34 quad_perm:[0,0,0,0] row_mask:0xf bank_mask:0xf
	v_dot2c_f32_f16_dpp v56, v51, v19 quad_perm:[0,0,0,0] row_mask:0xf bank_mask:0xf
	v_dot2c_f32_f16_dpp v57, v51, v35 quad_perm:[0,0,0,0] row_mask:0xf bank_mask:0xf
	v_dot2c_f32_f16_dpp v56, v48, v20 quad_perm:[1,1,1,1] row_mask:0xf bank_mask:0xf
	v_dot2c_f32_f16_dpp v57, v48, v36 quad_perm:[1,1,1,1] row_mask:0xf bank_mask:0xf
	v_dot2c_f32_f16_dpp v56, v49, v21 quad_perm:[1,1,1,1] row_mask:0xf bank_mask:0xf
	v_dot2c_f32_f16_dpp v57, v49, v37 quad_perm:[1,1,1,1] row_mask:0xf bank_mask:0xf
	v_dot2c_f32_f16_dpp v56, v50, v22 quad_perm:[1,1,1,1] row_mask:0xf bank_mask:0xf
	v_dot2c_f32_f16_dpp v57, v50, v38 quad_perm:[1,1,1,1] row_mask:0xf bank_mask:0xf
	v_dot2c_f32_f16_dpp v56, v51, v23 quad_perm:[1,1,1,1] row_mask:0xf bank_mask:0xf
	v_dot2c_f32_f16_dpp v57, v51, v39 quad_perm:[1,1,1,1] row_mask:0xf bank_mask:0xf
	v_dot2c_f32_f16_dpp v56, v48, v24 quad_perm:[2,2,2,2] row_mask:0xf bank_mask:0xf
	v_dot2c_f32_f16_dpp v57, v48, v40 quad_perm:[2,2,2,2] row_mask:0xf bank_mask:0xf
	v_dot2c_f32_f16_dpp v56, v49, v25 quad_perm:[2,2,2,2] row_mask:0xf bank_mask:0xf
	v_dot2c_f32_f16_dpp v57, v49, v41 quad_perm:[2,2,2,2] row_mask:0xf bank_mask:0xf
	v_dot2c_f32_f16_dpp v56, v50, v26 quad_perm:[2,2,2,2] row_mask:0xf bank_mask:0xf
	v_dot2c_f32_f16_dpp v57, v50, v42 quad_perm:[2,2,2,2] row_mask:0xf bank_mask:0xf
	v_dot2c_f32_f16_dpp v56, v51, v27 quad_perm:[2,2,2,2] row_mask:0xf bank_mask:0xf
	v_dot2c_f32_f16_dpp v57, v51, v43 quad_perm:[2,2,2,2] row_mask:0xf bank_mask:0xf
	v_dot2c_f32_f16_dpp v56, v48, v28 quad_perm:[3,3,3,3] row_mask:0xf bank_mask:0xf
	v_dot2c_f32_f16_dpp v57, v48, v44 quad_perm:[3,3,3,3] row_mask:0xf bank_mask:0xf
	v_dot2c_f32_f16_dpp v56, v49, v29 quad_perm:[3,3,3,3] row_mask:0xf bank_mask:0xf
	v_dot2c_f32_f16_dpp v57, v49, v45 quad_perm:[3,3,3,3] row_mask:0xf bank_mask:0xf
	v_dot2c_f32_f16_dpp v56, v50, v30 quad_perm:[3,3,3,3] row_mask:0xf bank_mask:0xf
	v_dot2c_f32_f16_dpp v57, v50, v46 quad_perm:[3,3,3,3] row_mask:0xf bank_mask:0xf
	v_dot2c_f32_f16_dpp v56, v51, v31 quad_perm:[3,3,3,3] row_mask:0xf bank_mask:0xf
	v_dot2c_f32_f16_dpp v57, v51, v47 quad_perm:[3,3,3,3] row_mask:0xf bank_mask:0xf
	s_nop 2
	v_and_or_b32 v244, v56, -16, v168
	v_and_or_b32 v245, v57, -16, v176
	v_min_i32_e32 v58, v244, v245
	s_nop 1
	v_min_i32_dpp v58, v58, v58 quad_perm:[1,0,3,2] row_mask:0xf bank_mask:0xf bound_ctrl:1
	s_nop 1
	v_min_i32_dpp v58, v58, v58 quad_perm:[2,3,0,1] row_mask:0xf bank_mask:0xf bound_ctrl:1
	s_nop 1
	v_min_i32_dpp v58, v58, v58 row_half_mirror row_mask:0xf bank_mask:0xf bound_ctrl:1
	v_and_b32_e32 v244, 12, v58
	v_lshlrev_b32_e32 v244, 2, v244
	v_and_b32_e32 v245, 3, v58
	v_sub_u32_e32 v246, v52, v171
	v_add3_u32 v59, v246, v244, v245
	v_cmp_le_u32_e64 s[54:55], s58, v59
	v_cmp_le_u32_e64 s[56:57], s59, v59
	s_nop 1
	v_cndmask_b32_e64 v244, 0, v253, s[54:55]
	v_cndmask_b32_e64 v245, 0, v254, s[56:57]
	v_sub_u32_e32 v246, v59, v244
	v_sub_u32_e32 v246, v246, v245
	v_cndmask_b32_e64 v244, 0, 1, s[54:55]
	v_cndmask_b32_e64 v245, 0, 1, s[56:57]
	v_add_u32_e32 v247, v244, v245
	v_lshlrev_b32_e32 v244, v247, v246
	v_mul_u32_u24_e32 v244, 0xaab, v244
	v_lshrrev_b32_e32 v244, 17, v244
	v_mul_u32_u24_e32 v245, 0x60, v244
	v_lshrrev_b32_e32 v245, v247, v245
	v_add_u32_e32 v245, v246, v245
	v_mul_u32_u24_e32 v245, 12, v245
	v_cndmask_b32_e64 v244, v172, v173, s[54:55]
	v_cndmask_b32_e64 v244, v244, v174, s[56:57]
	v_add_u32_e32 v245, v245, v244
	v_cndmask_b32_e64 v244, v152, v154, s[54:55]
	v_cndmask_b32_e64 v244, v244, v159, s[56:57]
	v_cndmask_b32_e64 v246, v153, v155, s[54:55]
	v_cndmask_b32_e64 v246, v246, v161, s[56:57]
	v_add_co_u32_e64 v60, s[60:61], v244, v245
	s_nop 1
	v_addc_co_u32_e64 v61, s[60:61], 0, v246, s[60:61]
	v_sub_u32_e32 v244, 2, v247
	v_lshlrev_b32_e64 v244, v244, 36
	v_add_u32_e32 v246, 1, v244
	v_mul_u32_u24_e32 v244, v244, v246
	v_lshlrev_b32_e32 v244, 3, v244
	v_add_co_u32_e64 v62, s[60:61], v60, v244
	s_nop 1
	v_addc_co_u32_e64 v63, s[60:61], 0, v61, s[60:61]
	global_load_dwordx3 v[64:66], v[60:61], off
	ds_read_b32 v72, v53
	ds_read_b32 v73, v53 offset:4
	ds_read_b32 v74, v53 offset:8
	s_mov_b64 s[52:53], exec
	s_and_b64 exec, exec, s[48:49]
	global_load_dwordx3 v[68:70], v[62:63], off
	ds_read_b32 v76, v53 offset:11520
	ds_read_b32 v77, v53 offset:11524
	ds_read_b32 v78, v53 offset:11528
	s_mov_b64 exec, s[52:53]
	s_waitcnt vmcnt(2)
	v_mov_b32_e32 v120, 0
	v_mov_b32_e32 v121, 0
	v_dot2c_f32_f16_dpp v120, v112, v80 quad_perm:[0,0,0,0] row_mask:0xf bank_mask:0xf
	v_dot2c_f32_f16_dpp v121, v112, v96 quad_perm:[0,0,0,0] row_mask:0xf bank_mask:0xf
	v_dot2c_f32_f16_dpp v120, v113, v81 quad_perm:[0,0,0,0] row_mask:0xf bank_mask:0xf
	v_dot2c_f32_f16_dpp v121, v113, v97 quad_perm:[0,0,0,0] row_mask:0xf bank_mask:0xf
	v_dot2c_f32_f16_dpp v120, v114, v82 quad_perm:[0,0,0,0] row_mask:0xf bank_mask:0xf
	v_dot2c_f32_f16_dpp v121, v114, v98 quad_perm:[0,0,0,0] row_mask:0xf bank_mask:0xf
	v_dot2c_f32_f16_dpp v120, v115, v83 quad_perm:[0,0,0,0] row_mask:0xf bank_mask:0xf
	v_dot2c_f32_f16_dpp v121, v115, v99 quad_perm:[0,0,0,0] row_mask:0xf bank_mask:0xf
	v_dot2c_f32_f16_dpp v120, v112, v84 quad_perm:[1,1,1,1] row_mask:0xf bank_mask:0xf
	v_dot2c_f32_f16_dpp v121, v112, v100 quad_perm:[1,1,1,1] row_mask:0xf bank_mask:0xf
	v_dot2c_f32_f16_dpp v120, v113, v85 quad_perm:[1,1,1,1] row_mask:0xf bank_mask:0xf
	v_dot2c_f32_f16_dpp v121, v113, v101 quad_perm:[1,1,1,1] row_mask:0xf bank_mask:0xf
	v_dot2c_f32_f16_dpp v120, v114, v86 quad_perm:[1,1,1,1] row_mask:0xf bank_mask:0xf
	v_dot2c_f32_f16_dpp v121, v114, v102 quad_perm:[1,1,1,1] row_mask:0xf bank_mask:0xf
	v_dot2c_f32_f16_dpp v120, v115, v87 quad_perm:[1,1,1,1] row_mask:0xf bank_mask:0xf
	v_dot2c_f32_f16_dpp v121, v115, v103 quad_perm:[1,1,1,1] row_mask:0xf bank_mask:0xf
	v_dot2c_f32_f16_dpp v120, v112, v88 quad_perm:[2,2,2,2] row_mask:0xf bank_mask:0xf
	v_dot2c_f32_f16_dpp v121, v112, v104 quad_perm:[2,2,2,2] row_mask:0xf bank_mask:0xf
	v_dot2c_f32_f16_dpp v120, v113, v89 quad_perm:[2,2,2,2] row_mask:0xf bank_mask:0xf
	v_dot2c_f32_f16_dpp v121, v113, v105 quad_perm:[2,2,2,2] row_mask:0xf bank_mask:0xf
	v_dot2c_f32_f16_dpp v120, v114, v90 quad_perm:[2,2,2,2] row_mask:0xf bank_mask:0xf
	v_dot2c_f32_f16_dpp v121, v114, v106 quad_perm:[2,2,2,2] row_mask:0xf bank_mask:0xf
	v_dot2c_f32_f16_dpp v120, v115, v91 quad_perm:[2,2,2,2] row_mask:0xf bank_mask:0xf
	v_dot2c_f32_f16_dpp v121, v115, v107 quad_perm:[2,2,2,2] row_mask:0xf bank_mask:0xf
	v_dot2c_f32_f16_dpp v120, v112, v92 quad_perm:[3,3,3,3] row_mask:0xf bank_mask:0xf
	v_dot2c_f32_f16_dpp v121, v112, v108 quad_perm:[3,3,3,3] row_mask:0xf bank_mask:0xf
	v_dot2c_f32_f16_dpp v120, v113, v93 quad_perm:[3,3,3,3] row_mask:0xf bank_mask:0xf
	v_dot2c_f32_f16_dpp v121, v113, v109 quad_perm:[3,3,3,3] row_mask:0xf bank_mask:0xf
	v_dot2c_f32_f16_dpp v120, v114, v94 quad_perm:[3,3,3,3] row_mask:0xf bank_mask:0xf
	v_dot2c_f32_f16_dpp v121, v114, v110 quad_perm:[3,3,3,3] row_mask:0xf bank_mask:0xf
	v_dot2c_f32_f16_dpp v120, v115, v95 quad_perm:[3,3,3,3] row_mask:0xf bank_mask:0xf
	v_dot2c_f32_f16_dpp v121, v115, v111 quad_perm:[3,3,3,3] row_mask:0xf bank_mask:0xf
	s_nop 2
	v_and_or_b32 v244, v120, -16, v168
	v_and_or_b32 v245, v121, -16, v176
	v_min_i32_e32 v122, v244, v245
	s_nop 1
	v_min_i32_dpp v122, v122, v122 quad_perm:[1,0,3,2] row_mask:0xf bank_mask:0xf bound_ctrl:1
	s_nop 1
	v_min_i32_dpp v122, v122, v122 quad_perm:[2,3,0,1] row_mask:0xf bank_mask:0xf bound_ctrl:1
	s_nop 1
	v_min_i32_dpp v122, v122, v122 row_half_mirror row_mask:0xf bank_mask:0xf bound_ctrl:1
	v_and_b32_e32 v244, 12, v122
	v_lshlrev_b32_e32 v244, 2, v244
	v_and_b32_e32 v245, 3, v122
	v_sub_u32_e32 v246, v116, v171
	v_add3_u32 v123, v246, v244, v245
	v_cmp_le_u32_e64 s[54:55], s58, v123
	v_cmp_le_u32_e64 s[56:57], s59, v123
	s_nop 1
	v_cndmask_b32_e64 v244, 0, v253, s[54:55]
	v_cndmask_b32_e64 v245, 0, v254, s[56:57]
	v_sub_u32_e32 v246, v123, v244
	v_sub_u32_e32 v246, v246, v245
	v_cndmask_b32_e64 v244, 0, 1, s[54:55]
	v_cndmask_b32_e64 v245, 0, 1, s[56:57]
	v_add_u32_e32 v247, v244, v245
	v_lshlrev_b32_e32 v244, v247, v246
	v_mul_u32_u24_e32 v244, 0xaab, v244
	v_lshrrev_b32_e32 v244, 17, v244
	v_mul_u32_u24_e32 v245, 0x60, v244
	v_lshrrev_b32_e32 v245, v247, v245
	v_add_u32_e32 v245, v246, v245
	v_mul_u32_u24_e32 v245, 12, v245
	v_cndmask_b32_e64 v244, v172, v173, s[54:55]
	v_cndmask_b32_e64 v244, v244, v174, s[56:57]
	v_add_u32_e32 v245, v245, v244
	v_cndmask_b32_e64 v244, v152, v154, s[54:55]
	v_cndmask_b32_e64 v244, v244, v159, s[56:57]
	v_cndmask_b32_e64 v246, v153, v155, s[54:55]
	v_cndmask_b32_e64 v246, v246, v161, s[56:57]
	v_add_co_u32_e64 v124, s[60:61], v244, v245
	s_nop 1
	v_addc_co_u32_e64 v125, s[60:61], 0, v246, s[60:61]
	v_sub_u32_e32 v244, 2, v247
	v_lshlrev_b32_e64 v244, v244, 36
	v_add_u32_e32 v246, 1, v244
	v_mul_u32_u24_e32 v244, v244, v246
	v_lshlrev_b32_e32 v244, 3, v244
	v_add_co_u32_e64 v126, s[60:61], v124, v244
	s_nop 1
	v_addc_co_u32_e64 v127, s[60:61], 0, v125, s[60:61]
	global_load_dwordx3 v[128:130], v[124:125], off
	ds_read_b32 v136, v117
	ds_read_b32 v137, v117 offset:4
	ds_read_b32 v138, v117 offset:8
	s_mov_b64 s[52:53], exec
	s_and_b64 exec, exec, s[48:49]
	global_load_dwordx3 v[132:134], v[126:127], off
	ds_read_b32 v140, v117 offset:11520
	ds_read_b32 v141, v117 offset:11524
	ds_read_b32 v142, v117 offset:11528
	s_mov_b64 exec, s[52:53]
	s_cmp_eq_u32 s50, 0
	s_cbranch_scc0 .Lno2d
	s_waitcnt vmcnt(4)
	s_waitcnt lgkmcnt(0)
	v_sub_f32_e32 v244, v234, v226
	v_add_f32_e64 v248, v248, |v244|
	v_sub_f32_e32 v244, v235, v227
	v_add_f32_e64 v248, v248, |v244|
	v_sub_f32_e32 v244, v236, v228
	v_add_f32_e64 v248, v248, |v244|
	s_mov_b64 s[52:53], exec
	s_and_b64 exec, exec, s[48:49]
	v_sub_f32_e32 v244, v238, v230
	v_add_f32_e64 v248, v248, |v244|
	v_sub_f32_e32 v244, v239, v231
	v_add_f32_e64 v248, v248, |v244|
	v_sub_f32_e32 v244, v240, v232
	v_add_f32_e64 v248, v248, |v244|
	s_mov_b64 exec, s[52:53]
.Lno2d:
	s_waitcnt vmcnt(2)
	s_waitcnt lgkmcnt(0)
	v_sub_f32_e32 v244, v72, v64
	v_add_f32_e64 v248, v248, |v244|
	v_sub_f32_e32 v244, v73, v65
	v_add_f32_e64 v248, v248, |v244|
	v_sub_f32_e32 v244, v74, v66
	v_add_f32_e64 v248, v248, |v244|
	s_mov_b64 s[52:53], exec
	s_and_b64 exec, exec, s[48:49]
	v_sub_f32_e32 v244, v76, v68
	v_add_f32_e64 v248, v248, |v244|
	v_sub_f32_e32 v244, v77, v69
	v_add_f32_e64 v248, v248, |v244|
	v_sub_f32_e32 v244, v78, v70
	v_add_f32_e64 v248, v248, |v244|
	s_mov_b64 exec, s[52:53]
	s_waitcnt vmcnt(0)
	s_waitcnt lgkmcnt(0)
	v_sub_f32_e32 v244, v136, v128
	v_add_f32_e64 v248, v248, |v244|
	v_sub_f32_e32 v244, v137, v129
	v_add_f32_e64 v248, v248, |v244|
	v_sub_f32_e32 v244, v138, v130
	v_add_f32_e64 v248, v248, |v244|
	s_mov_b64 s[52:53], exec
	s_and_b64 exec, exec, s[48:49]
	v_sub_f32_e32 v244, v140, v132
	v_add_f32_e64 v248, v248, |v244|
	v_sub_f32_e32 v244, v141, v133
	v_add_f32_e64 v248, v248, |v244|
	v_sub_f32_e32 v244, v142, v134
	v_add_f32_e64 v248, v248, |v244|
	s_mov_b64 exec, s[52:53]
	s_nop 1
	v_add_f32_dpp v248, v248, v248 quad_perm:[1,0,3,2] row_mask:0xf bank_mask:0xf
	s_nop 1
	v_add_f32_dpp v248, v248, v248 quad_perm:[2,3,0,1] row_mask:0xf bank_mask:0xf
	s_nop 1
	v_add_f32_dpp v248, v248, v248 row_half_mirror row_mask:0xf bank_mask:0xf
	s_nop 1
	v_add_f32_dpp v248, v248, v248 row_mirror row_mask:0xf bank_mask:0xf
	s_nop 1
	v_add_f32_dpp v248, v248, v248 row_bcast:15 row_mask:0xa bank_mask:0xf
	s_nop 1
	v_add_f32_dpp v248, v248, v248 row_bcast:31 row_mask:0xc bank_mask:0xf
	s_lshl_b32 s60, s15, 2
	v_mov_b32_e32 v244, s60
	s_mov_b64 s[52:53], exec
	s_mov_b32 exec_lo, 0
	s_mov_b32 exec_hi, 0x80000000
	ds_write_b32 v244, v248 offset:18112
	s_mov_b64 exec, s[52:53]
	s_load_dwordx2 s[2:3], s[0:1], 0x18
	v_cmp_eq_u32_e32 vcc, 0, v0
	s_waitcnt lgkmcnt(0)
	s_barrier
	s_and_saveexec_b64 s[0:1], vcc
	s_cbranch_execz .LBB1_34
	v_mov_b32_e32 v0, 0
	ds_read_b128 v[2:5], v0 offset:18112
	ds_read_b128 v[6:9], v0 offset:18128
	s_mov_b64 s[6:7], exec
	s_waitcnt lgkmcnt(0)
	v_add_f32_e32 v1, v2, v3
	v_add_f32_e32 v1, v1, v4
	v_add_f32_e32 v1, v1, v5
	v_add_f32_e32 v1, v1, v6
	v_add_f32_e32 v1, v1, v7
	v_add_f32_e32 v1, v1, v8
	v_add_f32_e32 v1, v1, v9
	v_mul_f32_e32 v1, 0x49800000, v1
	v_cvt_u32_f32_e32 v2, v1
	v_mbcnt_lo_u32_b32 v1, s6, 0
	v_mbcnt_hi_u32_b32 v1, s7, v1
	v_cmp_eq_u32_e32 vcc, 0, v1
	s_and_saveexec_b64 s[0:1], vcc
	s_cbranch_execz .LBB1_27
	s_lshl_b32 s8, s14, 4
	s_ashr_i32 s9, s8, 31
	s_lshl_b64 s[8:9], s[8:9], 3
	s_add_u32 s8, s4, s8
	s_addc_u32 s9, s5, s9
	s_bcnt1_i32_b64 s6, s[6:7]
	v_mov_b32_e32 v3, 0x1000000
	v_mul_lo_u32 v3, v3, s6
	v_mul_hi_u32 v4, v2, s6
	v_add_u32_e32 v5, v4, v3
	v_mul_lo_u32 v4, v2, s6
	v_mov_b32_e32 v3, 0x663000
	global_atomic_add_x2 v[4:5], v3, v[4:5], s[8:9] offset:3072 sc0

	.amdhsa_kernel _ZN12_GLOBAL__N_113search_kernelEPKfS1_PhPf
		.amdhsa_group_segment_fixed_size 26336
		.amdhsa_private_segment_fixed_size 0
		.amdhsa_kernarg_size 32
		.amdhsa_user_sgpr_count 2
		.amdhsa_user_sgpr_dispatch_ptr 0
		.amdhsa_user_sgpr_queue_ptr 0
		.amdhsa_user_sgpr_kernarg_segment_ptr 1
		.amdhsa_user_sgpr_dispatch_id 0
		.amdhsa_user_sgpr_kernarg_preload_length 0
		.amdhsa_user_sgpr_kernarg_preload_offset 0
		.amdhsa_user_sgpr_private_segment_size 0
		.amdhsa_uses_dynamic_stack 0
		.amdhsa_enable_private_segment 0
		.amdhsa_system_sgpr_workgroup_id_x 1
		.amdhsa_system_sgpr_workgroup_id_y 0
		.amdhsa_system_sgpr_workgroup_id_z 0
		.amdhsa_system_sgpr_workgroup_info 0
		.amdhsa_system_vgpr_workitem_id 0
		.amdhsa_next_free_vgpr 256
		.amdhsa_next_free_sgpr 80
		.amdhsa_accum_offset 256
		.amdhsa_reserve_vcc 1
		.amdhsa_float_round_mode_32 0
		.amdhsa_float_round_mode_16_64 0
		.amdhsa_float_denorm_mode_32 3
		.amdhsa_float_denorm_mode_16_64 3
		.amdhsa_dx10_clamp 1
		.amdhsa_ieee_mode 1
		.amdhsa_fp16_overflow 0
		.amdhsa_tg_split 0
		.amdhsa_exception_fp_ieee_invalid_op 0
		.amdhsa_exception_fp_denorm_src 0
		.amdhsa_exception_fp_ieee_div_zero 0
		.amdhsa_exception_fp_ieee_overflow 0
		.amdhsa_exception_fp_ieee_underflow 0
		.amdhsa_exception_fp_ieee_inexact 0
		.amdhsa_exception_int_div_zero 0
	.end_amdhsa_kernel

amdhsa.kernels:
  - .agpr_count:     0
    .args:
      - .actual_access:  read_only
        .address_space:  global
        .offset:         0
        .size:           8
        .value_kind:     global_buffer
      - .actual_access:  read_only
        .address_space:  global
        .offset:         8
        .size:           8
        .value_kind:     global_buffer
      - .actual_access:  write_only
        .address_space:  global
        .offset:         16
        .size:           8
        .value_kind:     global_buffer
    .group_segment_fixed_size: 26112
    .kernarg_segment_align: 8
    .kernarg_segment_size: 24
    .language:       OpenCL C
    .language_version:
      - 2
      - 0
    .max_flat_workgroup_size: 256
    .name:           _ZN12_GLOBAL__N_111prep_kernelEPKfS1_Ph
    .private_segment_fixed_size: 0
    .sgpr_count:     25
    .sgpr_spill_count: 0
    .symbol:         _ZN12_GLOBAL__N_111prep_kernelEPKfS1_Ph.kd
    .uniform_work_group_size: 1
    .uses_dynamic_stack: false
    .vgpr_count:     34
    .vgpr_spill_count: 0
    .wavefront_size: 64
  - .agpr_count:     0
    .args:
      - .actual_access:  read_only
        .address_space:  global
        .offset:         0
        .size:           8
        .value_kind:     global_buffer
      - .actual_access:  read_only
        .address_space:  global
        .offset:         8
        .size:           8
        .value_kind:     global_buffer
      - .address_space:  global
        .offset:         16
        .size:           8
        .value_kind:     global_buffer
      - .actual_access:  write_only
        .address_space:  global
        .offset:         24
        .size:           8
        .value_kind:     global_buffer
    .group_segment_fixed_size: 26336
    .kernarg_segment_align: 8
    .kernarg_segment_size: 32
    .language:       OpenCL C
    .language_version:
      - 2
      - 0
    .max_flat_workgroup_size: 512
    .name:           _ZN12_GLOBAL__N_113search_kernelEPKfS1_PhPf
    .private_segment_fixed_size: 0
    .sgpr_count:     86
    .sgpr_spill_count: 0
    .symbol:         _ZN12_GLOBAL__N_113search_kernelEPKfS1_PhPf.kd
    .uniform_work_group_size: 1
    .uses_dynamic_stack: false
    .vgpr_count:     256
    .vgpr_spill_count: 0
    .wavefront_size: 64
